# latent attention loop: LDS-DMA via scalar base (no VALU address adds), V LDS image in natural key order (drops 8 permlane swaps per tile), scalar lead tests
# speedup vs baseline: 1.0060x; 1.0060x over previous
; __device__ __forceinline__ void attn_dma_body(const bf16_t* __restrict__ Qb, int ldq, int tpos0, const float* __restrict__ rope, const float* __restrict__ qgain, ...
;     ...
;   unsigned koff[2], voff[2];
; #pragma unroll
;   for (int c = 0; c < 2; ++c) { const int g = c * 512 + tid;
;     { const int row = g >> 4, ch = (g & 15) ^ (row & 7); koff[c] = (unsigned)(row * 128 + ch * 8) * 2u; }
;     { const int sub = g >> 5, kk = (sub >> 2) * 8 + ((g >> 2) & 7), k = (kk & ~0xC) | ((kk & 4) << 1) | ((kk & 8) >> 1), col = (sub & 3) * 32 + (g & 3) * 8; voff[c] = (unsigned)(k * 128 + col) * 2u; } }
;   const unsigned wbase = (unsigned)__builtin_amdgcn_readfirstlane(wid) * 1024u;
;   typedef __attribute__((address_space(3))) unsigned lds_u32;
;   lds_u32* ldsl = (lds_u32*)(__attribute__((address_space(3))) char*)lds;
;     ...
;   const int NT = seq / KVBLK;
;   ATT_DMA(0, 0); ATT_DMA(1, 1);
; #pragma unroll
;   for (int d0 = 0; d0 < 8; ++d0) qr[d0] = ld8(Qw + d0 * 16);
;   if (tpos0 >= 0) {
;     float ss = 0.f;
; #pragma unroll
;     for (int d0 = 0; d0 < 8; ++d0)
; #pragma unroll
;       for (int i = 0; i < 8; ++i) { const float x = bf2f((unsigned)(unsigned short)qr[d0][i]); ss += x * x; }
;     { auto rr = __builtin_amdgcn_permlane32_swap(__float_as_uint(ss), __float_as_uint(ss), false, false); ss = __uint_as_float(rr[0]) + __uint_as_float(rr[1]); }
;     const float rinv = 1.0f / sqrtf(ss * (1.0f / 128.0f) + RMS_EPS);
;     const int t = tpos0 + wid * QBLK + r32;
; #pragma unroll
;     for (int ax = 0; ax < 2; ++ax) { const int pos = ax ? (t & 63) : (t >> 6);
; #pragma unroll
;       for (int q = 0; q < 2; ++q) { const int dl = 4 * ax + q, dh = dl + 2, p0 = q * 16 + 8 * hi;
;         const float* cp_ = rope + pos * 32 + p0; const float* gl = qgain + dl * 16 + 8 * hi; const float* gh = qgain + dh * 16 + 8 * hi;
;         float cs[8], sn[8], lo[8], hv[8];
; #pragma unroll
;         for (int i = 0; i < 8; ++i) { cs[i] = cp_[i]; sn[i] = cp_[4096 + i];
;           lo[i] = bf2f((unsigned)(unsigned short)qr[dl][i]) * rinv * gl[i]; hv[i] = bf2f((unsigned)(unsigned short)qr[dh][i]) * rinv * gh[i]; }
.LBB0_405:
	s_and_b64 vcc, exec, s[4:5]
	s_cbranch_vccz .LBB0_437
	v_mov_b32_e32 v147, v0
	s_mul_i32 s2, s71, 0x1800
	s_waitcnt vmcnt(0)
	v_and_b32_e32 v3, 0x60, v147
	v_lshlrev_b32_e32 v5, 3, v147
	v_and_b32_e32 v176, 15, v147
	v_lshrrev_b32_e32 v2, 2, v147
	v_and_or_b32 v3, v5, 24, v3
	v_ashrrev_i32_e32 v5, 4, v147
	v_bfe_u32 v146, v147, 2, 2
	v_and_b32_e32 v148, 4, v2
	v_bitop3_b32 v6, v5, v176, 7 bitop3:0x6c
	v_lshlrev_b32_e32 v149, 8, v5
	v_and_b32_e32 v154, 0xfffff0, v5
	v_or_b32_e32 v2, v148, v146
	v_and_b32_e32 v156, 8, v5
	s_mul_hi_u32 s3, s70, 0x1800
	v_lshlrev_b32_e32 v3, 1, v3
	v_or3_b32 v5, v154, v156, v2
	s_add_i32 s3, s3, s2
	s_mul_i32 s2, s70, 0x1800
	v_lshl_or_b32 v30, v5, 8, v3
	v_add_u32_e32 v5, 0x200, v147
	s_add_u32 s2, s22, s2
	v_ashrrev_i32_e32 v5, 4, v5
	s_addc_u32 s3, s88, s3
	s_lshl_b64 s[44:45], s[72:73], 1
	v_lshlrev_b32_e32 v150, 4, v6
	v_bitop3_b32 v6, v5, v176, 7 bitop3:0x6c
	v_lshlrev_b32_e32 v151, 8, v5
	v_and_b32_e32 v153, 0xfffff0, v5
	s_add_u32 s2, s2, s44
	v_ashrrev_i32_e32 v179, 6, v147
	v_and_b32_e32 v155, 8, v5
	s_addc_u32 s3, s3, s45
	v_and_b32_e32 v177, 31, v147
	v_lshlrev_b32_e32 v164, 5, v179
	v_or3_b32 v2, v153, v155, v2
	v_or_b32_e32 v4, v164, v177
	v_lshl_or_b32 v34, v2, 8, v3
	v_mov_b64_e32 v[2:3], s[2:3]
	s_movk_i32 s2, 0x1800
	v_mad_i64_i32 v[2:3], s[2:3], v4, s2, v[2:3]
	v_readfirstlane_b32 s2, v179
	s_lshl_b32 s2, s2, 10
	s_add_i32 s96, s2, 0
	v_or_b32_e32 v162, v150, v149
	s_add_i32 s2, s96, 0x4000
	s_mov_b32 m0, s96
	v_lshlrev_b32_e32 v152, 4, v6
	global_load_lds_dwordx4 v162, s[38:39]
	s_mov_b32 m0, s2
	v_or_b32_e32 v32, v152, v151
	global_load_lds_dwordx4 v30, s[40:41]
	s_add_i32 m0, s96, 0x2000
	v_bfe_u32 v178, v147, 5, 1
	global_load_lds_dwordx4 v32, s[38:39]
	s_add_i32 m0, s96, 0x6000
	s_add_u32 s2, s38, 0x4000
	s_addc_u32 s3, s39, 0
	s_add_u32 s4, s40, 0x4000
	global_load_lds_dwordx4 v34, s[40:41]
	s_addc_u32 s5, s41, 0
	s_add_i32 m0, s96, 0x8000
	s_add_i32 s6, s96, 0xc000
	global_load_lds_dwordx4 v162, s[2:3]
	s_mov_b32 m0, s6
	v_lshlrev_b32_e32 v166, 4, v178
	global_load_lds_dwordx4 v30, s[4:5]
	s_add_i32 m0, s96, 0xa000
	v_mov_b32_e32 v167, v163
	global_load_lds_dwordx4 v32, s[2:3]
	s_add_i32 m0, s96, 0xe000
	v_lshl_add_u64 v[2:3], v[2:3], 0, v[166:167]
	global_load_lds_dwordx4 v34, s[4:5]
	global_load_dwordx4 v[102:105], v[2:3], off
	global_load_dwordx4 v[110:113], v[2:3], off offset:32
	global_load_dwordx4 v[98:101], v[2:3], off offset:64
	global_load_dwordx4 v[106:109], v[2:3], off offset:96
	global_load_dwordx4 v[118:121], v[2:3], off offset:128
	global_load_dwordx4 v[126:129], v[2:3], off offset:160
	global_load_dwordx4 v[114:117], v[2:3], off offset:192
	global_load_dwordx4 v[122:125], v[2:3], off offset:224
	s_cmp_lt_i32 s68, 0
	s_cbranch_scc1 .LBB0_408
	v_lshl_or_b32 v3, s68, 8, v177
	v_lshlrev_b32_e32 v2, 3, v178
	v_add_u32_e32 v26, v3, v164
	v_lshlrev_b32_e32 v44, 2, v2
	v_ashrrev_i32_e32 v2, 1, v26
	v_and_b32_e32 v2, 0xffffffe0, v2
	v_ashrrev_i32_e32 v3, 31, v2
	v_mov_b32_e32 v45, v163
	v_lshl_add_u64 v[2:3], v[2:3], 2, s[16:17]
	v_lshl_add_u64 v[76:77], v[2:3], 0, v[44:45]
	s_mov_b64 s[2:3], 0x4000
	v_lshl_add_u64 v[6:7], v[76:77], 0, s[2:3]
	s_waitcnt lgkmcnt(0)
	global_load_dwordx4 v[130:133], v44, s[14:15] offset:16
	global_load_dwordx4 v[14:17], v44, s[14:15] offset:144
	global_load_dwordx4 v[2:5], v[76:77], off offset:16
	s_nop 0
	global_load_dwordx4 v[6:9], v[6:7], off offset:16
	s_nop 0
	global_load_dwordx4 v[22:25], v44, s[14:15]
	global_load_dwordx4 v[18:21], v44, s[14:15] offset:128
	s_waitcnt vmcnt(0)
	v_lshlrev_b32_e32 v38, 16, v129
	v_and_b32_e32 v36, 0xffff0000, v129
	v_lshlrev_b32_e32 v129, 16, v102
	v_lshlrev_b32_e32 v39, 16, v125
	v_and_b32_e32 v37, 0xffff0000, v125
	v_lshlrev_b32_e32 v49, 16, v123
	v_lshlrev_b32_e32 v48, 16, v127
	v_and_b32_e32 v47, 0xffff0000, v123
	v_and_b32_e32 v46, 0xffff0000, v127
	v_lshlrev_b32_e32 v123, 16, v99
	v_and_b32_e32 v127, 0xffff0000, v99
	v_and_b32_e32 v99, 0xffff0000, v102
	v_lshlrev_b32_e32 v53, 16, v122
	v_and_b32_e32 v51, 0xffff0000, v122
	v_lshlrev_b32_e32 v122, 16, v103
	v_lshlrev_b32_e32 v52, 16, v126
	v_and_b32_e32 v50, 0xffff0000, v126
	v_and_b32_e32 v126, 0xffff0000, v103
	v_lshlrev_b32_e32 v90, 16, v111
	v_and_b32_e32 v88, 0xffff0000, v111
	v_lshlrev_b32_e32 v92, 16, v110
	v_and_b32_e32 v94, 0xffff0000, v110
	v_lshlrev_b32_e32 v111, 16, v100
	v_lshlrev_b32_e32 v110, 16, v104
	v_lshlrev_b32_e32 v65, 16, v116
	v_and_b32_e32 v63, 0xffff0000, v116
	v_lshlrev_b32_e32 v73, 16, v114
	v_and_b32_e32 v71, 0xffff0000, v114
	v_lshlrev_b32_e32 v114, 16, v105
	v_and_b32_e32 v116, 0xffff0000, v105
	v_and_b32_e32 v105, 0xffff0000, v100
	v_and_b32_e32 v104, 0xffff0000, v104
	v_lshlrev_b32_e32 v69, 16, v115
	v_and_b32_e32 v67, 0xffff0000, v115
	v_lshlrev_b32_e32 v115, 16, v101
	v_lshlrev_b32_e32 v61, 16, v117
	v_and_b32_e32 v55, 0xffff0000, v117
	v_and_b32_e32 v117, 0xffff0000, v101
	v_lshlrev_b32_e32 v93, 16, v106
	v_and_b32_e32 v95, 0xffff0000, v106
	v_lshlrev_b32_e32 v91, 16, v107
	v_and_b32_e32 v89, 0xffff0000, v107
	v_lshlrev_b32_e32 v87, 16, v108
	v_lshlrev_b32_e32 v86, 16, v112
	v_and_b32_e32 v85, 0xffff0000, v108
	v_and_b32_e32 v84, 0xffff0000, v112
	v_lshlrev_b32_e32 v83, 16, v109
	v_lshlrev_b32_e32 v82, 16, v113
	v_and_b32_e32 v81, 0xffff0000, v109
	v_and_b32_e32 v80, 0xffff0000, v113
	v_lshlrev_b32_e32 v42, 16, v128
	v_and_b32_e32 v40, 0xffff0000, v128
	v_lshlrev_b32_e32 v128, 16, v98
	v_and_b32_e32 v98, 0xffff0000, v98
	s_movk_i32 s4, 0x4000
	v_lshlrev_b32_e32 v26, 7, v26
	v_add_co_u32_e32 v78, vcc, s4, v76
	v_mov_b32_e32 v27, v163
	v_and_b32_e32 v26, 0x1f80, v26
	v_addc_co_u32_e32 v79, vcc, 0, v77, vcc
; __device__ __forceinline__ void attn_dma_body(const bf16_t* __restrict__ Qb, int ldq, int tpos0, const float* __restrict__ rope, const float* __restrict__ qgain, ...
;     ...
;     float ss = 0.f;
; #pragma unroll
;     for (int d0 = 0; d0 < 8; ++d0)
; #pragma unroll
;       for (int i = 0; i < 8; ++i) { const float x = bf2f((unsigned)(unsigned short)qr[d0][i]); ss += x * x; }
;     { auto rr = __builtin_amdgcn_permlane32_swap(__float_as_uint(ss), __float_as_uint(ss), false, false); ss = __uint_as_float(rr[0]) + __uint_as_float(rr[1]); }
;     const float rinv = 1.0f / sqrtf(ss * (1.0f / 128.0f) + RMS_EPS);
	v_lshl_add_u64 v[26:27], s[16:17], 0, v[26:27]
	global_load_dwordx4 v[10:13], v[78:79], off
	v_lshl_add_u64 v[58:59], v[26:27], 0, v[44:45]
	global_load_dwordx4 v[26:29], v[76:77], off
	v_lshlrev_b32_e32 v72, 16, v118
	v_and_b32_e32 v70, 0xffff0000, v118
	v_lshlrev_b32_e32 v68, 16, v119
	v_and_b32_e32 v66, 0xffff0000, v119
	v_lshlrev_b32_e32 v64, 16, v120
	v_and_b32_e32 v62, 0xffff0000, v120
	v_lshlrev_b32_e32 v60, 16, v121
	v_and_b32_e32 v54, 0xffff0000, v121
	v_lshlrev_b32_e32 v43, 16, v124
	v_and_b32_e32 v41, 0xffff0000, v124
	v_mov_b32_e32 v134, v37
	v_mov_b32_e32 v135, v39
	v_lshl_add_u64 v[74:75], v[58:59], 0, s[2:3]
	v_mov_b32_e32 v125, v20
	v_mul_f32_e32 v20, v129, v129
	v_fmac_f32_e32 v20, v99, v99
	v_pk_fma_f32 v[102:103], v[122:123], v[122:123], v[20:21] op_sel_hi:[1,1,0]
	v_mul_f32_e32 v20, v123, v123
	v_pk_fma_f32 v[102:103], v[126:127], v[126:127], v[102:103]
	s_mov_b32 s2, 0xf800000
	v_pk_fma_f32 v[102:103], v[110:111], v[110:111], v[102:103]
	v_mov_b32_e32 v124, v24
	v_pk_fma_f32 v[102:103], v[104:105], v[104:105], v[102:103]
	v_mov_b32_e32 v120, v130
	v_pk_fma_f32 v[102:103], v[114:115], v[114:115], v[102:103]
	v_mov_b32_e32 v121, v14
	v_pk_fma_f32 v[102:103], v[116:117], v[116:117], v[102:103]
	v_mov_b32_e32 v14, v131
	v_pk_fma_f32 v[102:103], v[92:93], v[92:93], v[102:103]
	v_mov_b32_e32 v118, v132
	v_pk_fma_f32 v[102:103], v[94:95], v[94:95], v[102:103]
	v_mov_b32_e32 v119, v16
	v_pk_fma_f32 v[102:103], v[90:91], v[90:91], v[102:103]
	v_mov_b32_e32 v16, v133
	v_pk_fma_f32 v[102:103], v[88:89], v[88:89], v[102:103]
	v_mov_b32_e32 v106, v6
	v_pk_fma_f32 v[102:103], v[86:87], v[86:87], v[102:103]
	v_mov_b32_e32 v107, v2
	v_pk_fma_f32 v[102:103], v[84:85], v[84:85], v[102:103]
	v_lshl_add_u64 v[96:97], v[76:77], 0, s[24:25]
	v_pk_fma_f32 v[102:103], v[82:83], v[82:83], v[102:103]
	v_mov_b32_e32 v112, v8
	v_pk_fma_f32 v[102:103], v[80:81], v[80:81], v[102:103]
	v_mov_b32_e32 v113, v4
	v_pk_fma_f32 v[102:103], v[128:129], v[128:129], v[102:103]
	v_mov_b32_e32 v108, v9
	v_pk_fma_f32 v[102:103], v[98:99], v[98:99], v[102:103]
	v_mov_b32_e32 v109, v5
	v_pk_add_f32 v[102:103], v[20:21], v[102:103] op_sel_hi:[0,1]
	v_mul_f32_e32 v20, v127, v127
	v_pk_add_f32 v[102:103], v[20:21], v[102:103] op_sel_hi:[0,1]
	v_mul_f32_e32 v20, v111, v111
	v_pk_add_f32 v[102:103], v[20:21], v[102:103] op_sel_hi:[0,1]
	v_mul_f32_e32 v20, v105, v105
	v_pk_add_f32 v[102:103], v[20:21], v[102:103] op_sel_hi:[0,1]
	v_mul_f32_e32 v20, v115, v115
	v_pk_add_f32 v[102:103], v[20:21], v[102:103] op_sel_hi:[0,1]
	v_mul_f32_e32 v20, v117, v117
	v_pk_add_f32 v[102:103], v[20:21], v[102:103] op_sel_hi:[0,1]
	v_mul_f32_e32 v20, v93, v93
	v_pk_add_f32 v[102:103], v[20:21], v[102:103] op_sel_hi:[0,1]
	v_mul_f32_e32 v20, v95, v95
	v_pk_add_f32 v[102:103], v[20:21], v[102:103] op_sel_hi:[0,1]
	v_mul_f32_e32 v20, v91, v91
	v_pk_add_f32 v[102:103], v[20:21], v[102:103] op_sel_hi:[0,1]
	v_mul_f32_e32 v20, v89, v89
	v_pk_add_f32 v[102:103], v[20:21], v[102:103] op_sel_hi:[0,1]
	v_mul_f32_e32 v20, v87, v87
	v_pk_add_f32 v[102:103], v[20:21], v[102:103] op_sel_hi:[0,1]
	v_mul_f32_e32 v20, v85, v85
	v_pk_add_f32 v[102:103], v[20:21], v[102:103] op_sel_hi:[0,1]
	v_mul_f32_e32 v20, v83, v83
	v_pk_add_f32 v[102:103], v[20:21], v[102:103] op_sel_hi:[0,1]
	v_mul_f32_e32 v20, v81, v81
	v_pk_add_f32 v[102:103], v[20:21], v[102:103] op_sel_hi:[0,1]
	v_pk_fma_f32 v[102:103], v[72:73], v[72:73], v[102:103]
	v_mul_f32_e32 v20, v73, v73
	v_pk_fma_f32 v[102:103], v[70:71], v[70:71], v[102:103]
	s_waitcnt vmcnt(1)
	v_mov_b32_e32 v100, v12
	v_pk_fma_f32 v[102:103], v[68:69], v[68:69], v[102:103]
	s_waitcnt vmcnt(0)
	v_mov_b32_e32 v101, v28
	v_pk_fma_f32 v[102:103], v[66:67], v[66:67], v[102:103]
	v_lshl_add_u64 v[56:57], v[58:59], 0, s[24:25]
	v_pk_fma_f32 v[102:103], v[64:65], v[64:65], v[102:103]
	s_nop 0
	v_pk_fma_f32 v[102:103], v[62:63], v[62:63], v[102:103]
	s_nop 0
	v_pk_fma_f32 v[102:103], v[60:61], v[60:61], v[102:103]
	s_nop 0
	v_pk_fma_f32 v[102:103], v[54:55], v[54:55], v[102:103]
	s_nop 0
	v_pk_fma_f32 v[102:103], v[52:53], v[52:53], v[102:103]
	s_nop 0
	v_pk_fma_f32 v[102:103], v[50:51], v[50:51], v[102:103]
	s_nop 0
	v_pk_fma_f32 v[102:103], v[48:49], v[48:49], v[102:103]
	s_nop 0
	v_pk_fma_f32 v[102:103], v[46:47], v[46:47], v[102:103]
	s_nop 0
	v_pk_fma_f32 v[102:103], v[42:43], v[42:43], v[102:103]
	s_nop 0
	v_pk_fma_f32 v[102:103], v[40:41], v[40:41], v[102:103]
	s_nop 0
	v_pk_fma_f32 v[102:103], v[38:39], v[38:39], v[102:103]
	s_nop 0
	v_pk_fma_f32 v[102:103], v[36:37], v[36:37], v[102:103]
	s_nop 0
	v_pk_add_f32 v[102:103], v[20:21], v[102:103] op_sel_hi:[0,1]
	v_mul_f32_e32 v20, v71, v71
	v_pk_add_f32 v[102:103], v[20:21], v[102:103] op_sel_hi:[0,1]
	v_mul_f32_e32 v20, v69, v69
	v_pk_add_f32 v[102:103], v[20:21], v[102:103] op_sel_hi:[0,1]
	v_mul_f32_e32 v20, v67, v67
	v_pk_add_f32 v[102:103], v[20:21], v[102:103] op_sel_hi:[0,1]
	v_mul_f32_e32 v20, v65, v65
	v_pk_add_f32 v[102:103], v[20:21], v[102:103] op_sel_hi:[0,1]
	v_mul_f32_e32 v20, v63, v63
	v_pk_add_f32 v[102:103], v[20:21], v[102:103] op_sel_hi:[0,1]
	v_mul_f32_e32 v20, v61, v61
	v_pk_add_f32 v[102:103], v[20:21], v[102:103] op_sel_hi:[0,1]
	v_mul_f32_e32 v20, v55, v55
	v_pk_add_f32 v[102:103], v[20:21], v[102:103] op_sel_hi:[0,1]
	v_mul_f32_e32 v20, v53, v53
	v_pk_add_f32 v[102:103], v[20:21], v[102:103] op_sel_hi:[0,1]
	v_mul_f32_e32 v20, v51, v51
	v_pk_add_f32 v[102:103], v[20:21], v[102:103] op_sel_hi:[0,1]
	v_mul_f32_e32 v20, v49, v49
	v_pk_add_f32 v[102:103], v[20:21], v[102:103] op_sel_hi:[0,1]
	v_mul_f32_e32 v20, v47, v47
	v_pk_add_f32 v[102:103], v[20:21], v[102:103] op_sel_hi:[0,1]
; __device__ __forceinline__ unsigned pk2(float lo, float hi) { unsigned r; asm("v_cvt_pk_bf16_f32 %0, %1, %2" : "=v"(r) : "v"(lo), "v"(hi)); return r; }
; __device__ __forceinline__ void attn_dma_body(const bf16_t* __restrict__ Qb, int ldq, int tpos0, const float* __restrict__ rope, const float* __restrict__ qgain, ...
;     ...
;     const float rinv = 1.0f / sqrtf(ss * (1.0f / 128.0f) + RMS_EPS);
;     const int t = tpos0 + wid * QBLK + r32;
; #pragma unroll
;     for (int ax = 0; ax < 2; ++ax) { const int pos = ax ? (t & 63) : (t >> 6);
; #pragma unroll
;       for (int q = 0; q < 2; ++q) { const int dl = 4 * ax + q, dh = dl + 2, p0 = q * 16 + 8 * hi;
;         const float* cp_ = rope + pos * 32 + p0; const float* gl = qgain + dl * 16 + 8 * hi; const float* gh = qgain + dh * 16 + 8 * hi;
;         float cs[8], sn[8], lo[8], hv[8];
; #pragma unroll
;         for (int i = 0; i < 8; ++i) { cs[i] = cp_[i]; sn[i] = cp_[4096 + i];
;           lo[i] = bf2f((unsigned)(unsigned short)qr[dl][i]) * rinv * gl[i]; hv[i] = bf2f((unsigned)(unsigned short)qr[dh][i]) * rinv * gh[i]; }
;         u32x4 wl, wh;
; #pragma unroll
;         for (int i = 0; i < 4; ++i) { const float l0 = lo[2 * i] * cs[2 * i] - hv[2 * i] * sn[2 * i], l1 = lo[2 * i + 1] * cs[2 * i + 1] - hv[2 * i + 1] * sn[2 * i + 1];
;           const float h0 = hv[2 * i] * cs[2 * i] + lo[2 * i] * sn[2 * i], h1 = hv[2 * i + 1] * cs[2 * i + 1] + lo[2 * i + 1] * sn[2 * i + 1];
;           wl[i] = pk2(l0, l1); wh[i] = pk2(h0, h1); }
;         qr[dl] = *reinterpret_cast<bf16x8*>(&wl); qr[dh] = *reinterpret_cast<bf16x8*>(&wh); } } }
	v_mul_f32_e32 v20, v43, v43
	v_pk_add_f32 v[102:103], v[20:21], v[102:103] op_sel_hi:[0,1]
	v_mul_f32_e32 v20, v41, v41
	v_pk_add_f32 v[102:103], v[20:21], v[102:103] op_sel_hi:[0,1]
	v_mul_f32_e32 v20, v39, v39
	v_pk_add_f32 v[102:103], v[20:21], v[102:103] op_sel_hi:[0,1]
	v_pk_fma_f32 v[102:103], v[134:135], v[134:135], v[102:103]
	global_load_dwordx4 v[130:133], v44, s[14:15] offset:80
	global_load_dwordx4 v[134:137], v44, s[14:15] offset:64
	global_load_dwordx4 v[138:141], v44, s[14:15] offset:208
	global_load_dwordx4 v[142:145], v44, s[14:15] offset:192
	v_mov_b32_e32 v20, v102
	s_nop 1
	v_permlane32_swap_b32_e32 v102, v20
	v_add_f32_e32 v20, v102, v20
	v_fmamk_f32 v20, v20, 0x3c000000, v1
	v_mul_f32_e32 v24, 0x4f800000, v20
	v_cmp_gt_f32_e32 vcc, s2, v20
	v_mov_b32_e32 v102, v26
	v_mov_b32_e32 v103, v10
	v_cndmask_b32_e32 v31, v20, v24, vcc
	v_sqrt_f32_e32 v33, v31
	v_mov_b32_e32 v24, v18
	v_mov_b32_e32 v20, v25
	v_add_u32_e32 v18, -1, v33
	v_fma_f32 v25, -v18, v33, v31
	v_cmp_ge_f32_e64 s[2:3], 0, v25
	v_add_u32_e32 v25, 1, v33
	s_nop 0
	v_cndmask_b32_e64 v18, v33, v18, s[2:3]
	v_fma_f32 v33, -v25, v33, v31
	v_cmp_lt_f32_e64 s[2:3], 0, v33
	s_nop 1
	v_cndmask_b32_e64 v18, v18, v25, s[2:3]
	v_mul_f32_e32 v25, 0x37800000, v18
	v_cndmask_b32_e32 v18, v18, v25, vcc
	v_cmp_class_f32_e32 vcc, v31, v174
	v_mov_b32_e32 v25, v22
	s_nop 0
	v_cndmask_b32_e32 v18, v18, v31, vcc
	v_div_scale_f32 v31, s[2:3], v18, v18, 1.0
	v_rcp_f32_e32 v33, v31
	s_nop 0
	v_fma_f32 v22, -v31, v33, 1.0
	v_fmac_f32_e32 v33, v22, v33
	v_div_scale_f32 v22, vcc, 1.0, v18, 1.0
	v_mul_f32_e32 v35, v22, v33
	v_fma_f32 v45, -v31, v35, v22
	v_fmac_f32_e32 v35, v45, v33
	v_fma_f32 v22, -v31, v35, v22
	v_div_fmas_f32 v22, v22, v33, v35
	v_div_fixup_f32 v18, v22, v18, 1.0
	v_pk_mul_f32 v[98:99], v[18:19], v[98:99] op_sel_hi:[0,1]
	v_mov_b32_e32 v22, v19
	v_pk_mul_f32 v[98:99], v[98:99], v[22:23]
	v_pk_mul_f32 v[22:23], v[18:19], v[122:123] op_sel_hi:[0,1]
	v_pk_mul_f32 v[122:123], v[22:23], v[124:125]
	v_pk_mul_f32 v[22:23], v[18:19], v[126:127] op_sel_hi:[0,1]
	v_pk_mul_f32 v[124:125], v[22:23], v[20:21]
	v_pk_mul_f32 v[20:21], v[18:19], v[110:111] op_sel_hi:[0,1]
	v_pk_mul_f32 v[110:111], v[20:21], v[120:121]
	v_pk_mul_f32 v[20:21], v[18:19], v[104:105] op_sel_hi:[0,1]
	v_pk_mul_f32 v[104:105], v[20:21], v[14:15]
	v_pk_mul_f32 v[14:15], v[18:19], v[114:115] op_sel_hi:[0,1]
	v_pk_mul_f32 v[128:129], v[18:19], v[128:129] op_sel_hi:[0,1]
	v_pk_mul_f32 v[114:115], v[14:15], v[118:119]
	v_pk_mul_f32 v[14:15], v[18:19], v[116:117] op_sel_hi:[0,1]
	v_pk_mul_f32 v[24:25], v[24:25], v[128:129]
	v_pk_mul_f32 v[116:117], v[14:15], v[16:17]
	v_mov_b32_e32 v14, v10
	v_mov_b32_e32 v15, v26
	v_pk_mul_f32 v[14:15], v[14:15], v[24:25]
	v_mov_b32_e32 v26, v11
	v_sub_f32_e32 v19, v15, v14
	v_pk_mul_f32 v[14:15], v[26:27], v[98:99]
	v_mov_b32_e32 v10, v27
	v_sub_f32_e32 v31, v15, v14
	v_pk_mul_f32 v[14:15], v[102:103], v[24:25]
	v_pk_mul_f32 v[10:11], v[10:11], v[98:99]
	v_add_f32_e32 v33, v14, v15
	global_load_dwordx4 v[14:17], v[76:77], off offset:80
	global_load_dwordx4 v[20:23], v[76:77], off offset:64
	global_load_dwordx4 v[24:27], v[78:79], off offset:64
	v_add_f32_e32 v10, v10, v11
	v_cvt_pk_bf16_f32 v98, v33, v10
	v_mov_b32_e32 v10, v28
	v_mov_b32_e32 v11, v12
	v_pk_mul_f32 v[10:11], v[10:11], v[122:123]
	v_mov_b32_e32 v12, v29
	v_cvt_pk_bf16_f32 v102, v19, v31
	v_sub_f32_e32 v19, v10, v11
	v_pk_mul_f32 v[10:11], v[12:13], v[124:125]
	v_mov_b32_e32 v28, v13
	v_sub_f32_e32 v12, v10, v11
	v_pk_mul_f32 v[10:11], v[100:101], v[122:123]
	v_cvt_pk_bf16_f32 v103, v19, v12
	s_waitcnt vmcnt(3)
	v_mov_b32_e32 v13, v144
	v_add_f32_e32 v31, v10, v11
	v_pk_mul_f32 v[10:11], v[28:29], v[124:125]
	v_mov_b32_e32 v144, v137
	v_add_f32_e32 v10, v10, v11
	v_cvt_pk_bf16_f32 v99, v31, v10
	v_mov_b32_e32 v10, v2
	v_mov_b32_e32 v11, v6
	v_pk_mul_f32 v[10:11], v[10:11], v[110:111]
	v_mov_b32_e32 v6, v3
	v_mov_b32_e32 v2, v7
	v_sub_f32_e32 v12, v10, v11
	v_pk_mul_f32 v[10:11], v[6:7], v[104:105]
	v_pk_mul_f32 v[2:3], v[2:3], v[104:105]
	v_sub_f32_e32 v6, v10, v11
	v_pk_mul_f32 v[10:11], v[106:107], v[110:111]
	v_add_f32_e32 v2, v2, v3
	v_add_f32_e32 v10, v10, v11
	v_cvt_pk_bf16_f32 v100, v10, v2
	v_mov_b32_e32 v2, v4
	v_mov_b32_e32 v3, v8
	v_pk_mul_f32 v[2:3], v[2:3], v[114:115]
	v_mov_b32_e32 v8, v5
	v_cvt_pk_bf16_f32 v104, v12, v6
	v_sub_f32_e32 v4, v2, v3
	v_pk_mul_f32 v[2:3], v[8:9], v[116:117]
	global_load_dwordx4 v[6:9], v[96:97], off offset:16
	v_sub_f32_e32 v5, v2, v3
	v_pk_mul_f32 v[2:3], v[112:113], v[114:115]
	v_mov_b32_e32 v12, v136
	v_add_f32_e32 v10, v2, v3
	v_pk_mul_f32 v[2:3], v[108:109], v[116:117]
	v_cvt_pk_bf16_f32 v105, v4, v5
	v_mov_b32_e32 v4, v134
	v_add_f32_e32 v2, v2, v3
	v_cvt_pk_bf16_f32 v101, v10, v2
	v_pk_mul_f32 v[10:11], v[18:19], v[90:91] op_sel_hi:[0,1]
	v_pk_mul_f32 v[28:29], v[10:11], v[12:13]
	v_pk_mul_f32 v[10:11], v[18:19], v[88:89] op_sel_hi:[0,1]
	v_pk_mul_f32 v[96:97], v[10:11], v[144:145]
	v_pk_mul_f32 v[10:11], v[18:19], v[86:87] op_sel_hi:[0,1]
	v_mov_b32_e32 v12, v130
	v_mov_b32_e32 v13, v138
	v_pk_mul_f32 v[2:3], v[18:19], v[92:93] op_sel_hi:[0,1]
	v_mov_b32_e32 v5, v142
	v_pk_mul_f32 v[108:109], v[10:11], v[12:13]
	v_mov_b32_e32 v13, v140
	v_pk_mul_f32 v[88:89], v[18:19], v[80:81] op_sel_hi:[0,1]
	v_mov_b32_e32 v140, v133
	v_pk_mul_f32 v[2:3], v[2:3], v[4:5]
	v_pk_mul_f32 v[116:117], v[88:89], v[140:141]
	v_pk_mul_f32 v[4:5], v[18:19], v[94:95] op_sel_hi:[0,1]
	v_mov_b32_e32 v142, v135
	v_pk_mul_f32 v[10:11], v[18:19], v[84:85] op_sel_hi:[0,1]
	v_mov_b32_e32 v138, v131
	v_pk_mul_f32 v[4:5], v[4:5], v[142:143]
	v_pk_mul_f32 v[112:113], v[10:11], v[138:139]
	v_pk_mul_f32 v[10:11], v[18:19], v[82:83] op_sel_hi:[0,1]
	v_mov_b32_e32 v12, v132
	v_pk_mul_f32 v[114:115], v[10:11], v[12:13]
	global_load_dwordx4 v[10:13], v44, s[14:15] offset:272
	global_load_dwordx4 v[76:79], v44, s[14:15] offset:256
	global_load_dwordx4 v[80:83], v44, s[14:15] offset:400
	global_load_dwordx4 v[84:87], v44, s[14:15] offset:384
	v_add_co_u32_e32 v118, vcc, s4, v58
	s_waitcnt vmcnt(6)
; __device__ __forceinline__ unsigned pk2(float lo, float hi) { unsigned r; asm("v_cvt_pk_bf16_f32 %0, %1, %2" : "=v"(r) : "v"(lo), "v"(hi)); return r; }
; __device__ __forceinline__ void attn_dma_body(const bf16_t* __restrict__ Qb, int ldq, int tpos0, const float* __restrict__ rope, const float* __restrict__ qgain, ...
;     ...
;     for (int ax = 0; ax < 2; ++ax) { const int pos = ax ? (t & 63) : (t >> 6);
; #pragma unroll
;       for (int q = 0; q < 2; ++q) { const int dl = 4 * ax + q, dh = dl + 2, p0 = q * 16 + 8 * hi;
;         const float* cp_ = rope + pos * 32 + p0; const float* gl = qgain + dl * 16 + 8 * hi; const float* gh = qgain + dh * 16 + 8 * hi;
;         float cs[8], sn[8], lo[8], hv[8];
; #pragma unroll
;         for (int i = 0; i < 8; ++i) { cs[i] = cp_[i]; sn[i] = cp_[4096 + i];
;           lo[i] = bf2f((unsigned)(unsigned short)qr[dl][i]) * rinv * gl[i]; hv[i] = bf2f((unsigned)(unsigned short)qr[dh][i]) * rinv * gh[i]; }
;         u32x4 wl, wh;
; #pragma unroll
;         for (int i = 0; i < 4; ++i) { const float l0 = lo[2 * i] * cs[2 * i] - hv[2 * i] * sn[2 * i], l1 = lo[2 * i + 1] * cs[2 * i + 1] - hv[2 * i + 1] * sn[2 * i + 1];
;           const float h0 = hv[2 * i] * cs[2 * i] + lo[2 * i] * sn[2 * i], h1 = hv[2 * i + 1] * cs[2 * i + 1] + lo[2 * i + 1] * sn[2 * i + 1];
;           wl[i] = pk2(l0, l1); wh[i] = pk2(h0, h1); }
;         qr[dl] = *reinterpret_cast<bf16x8*>(&wl); qr[dh] = *reinterpret_cast<bf16x8*>(&wh); } } }
	v_mov_b32_e32 v88, v20
	s_waitcnt vmcnt(5)
	v_mov_b32_e32 v89, v24
	v_pk_mul_f32 v[88:89], v[88:89], v[2:3]
	v_addc_co_u32_e32 v119, vcc, 0, v59, vcc
	v_sub_f32_e32 v19, v88, v89
	v_mov_b32_e32 v88, v21
	v_mov_b32_e32 v89, v25
	v_pk_mul_f32 v[88:89], v[88:89], v[4:5]
	s_nop 0
	v_sub_f32_e32 v31, v88, v89
	v_mov_b32_e32 v88, v24
	v_mov_b32_e32 v89, v20
	v_pk_mul_f32 v[2:3], v[88:89], v[2:3]
	v_mov_b32_e32 v20, v25
	v_add_f32_e32 v24, v2, v3
	v_pk_mul_f32 v[2:3], v[20:21], v[4:5]
	v_cvt_pk_bf16_f32 v110, v19, v31
	s_nop 0
	v_add_f32_e32 v2, v2, v3
	v_cvt_pk_bf16_f32 v106, v24, v2
	v_mov_b32_e32 v2, v22
	v_mov_b32_e32 v3, v26
	v_pk_mul_f32 v[2:3], v[2:3], v[28:29]
	s_nop 0
	v_sub_f32_e32 v19, v2, v3
	v_mov_b32_e32 v2, v23
	v_mov_b32_e32 v3, v27
	v_pk_mul_f32 v[20:21], v[2:3], v[96:97]
	global_load_dwordx4 v[2:5], v[58:59], off offset:16
	global_load_dwordx4 v[88:91], v[58:59], off
	global_load_dwordx4 v[92:95], v[118:119], off
	v_sub_f32_e32 v24, v20, v21
	v_mov_b32_e32 v20, v26
	v_mov_b32_e32 v21, v22
	v_pk_mul_f32 v[20:21], v[20:21], v[28:29]
	v_mov_b32_e32 v22, v27
	v_add_f32_e32 v25, v20, v21
	v_pk_mul_f32 v[20:21], v[22:23], v[96:97]
	v_cvt_pk_bf16_f32 v111, v19, v24
	s_nop 0
	v_add_f32_e32 v20, v20, v21
	v_cvt_pk_bf16_f32 v107, v25, v20
	v_mov_b32_e32 v20, v14
	s_waitcnt vmcnt(7)
	v_mov_b32_e32 v21, v6
	v_pk_mul_f32 v[20:21], v[20:21], v[108:109]
	s_nop 0
	v_sub_f32_e32 v19, v20, v21
	v_mov_b32_e32 v20, v15
	v_mov_b32_e32 v21, v7
	v_pk_mul_f32 v[20:21], v[20:21], v[112:113]
	s_nop 0
	v_sub_f32_e32 v22, v20, v21
	v_mov_b32_e32 v21, v14
	v_mov_b32_e32 v14, v7
	v_mov_b32_e32 v20, v6
	v_pk_mul_f32 v[6:7], v[14:15], v[112:113]
	v_pk_mul_f32 v[20:21], v[20:21], v[108:109]
	v_add_f32_e32 v6, v6, v7
	v_add_f32_e32 v20, v20, v21
	v_cvt_pk_bf16_f32 v108, v20, v6
	v_mov_b32_e32 v6, v16
	v_mov_b32_e32 v7, v8
	v_cvt_pk_bf16_f32 v112, v19, v22
	v_pk_mul_f32 v[6:7], v[6:7], v[114:115]
	global_load_dwordx4 v[20:23], v[74:75], off offset:16
	v_sub_f32_e32 v14, v6, v7
	v_mov_b32_e32 v6, v17
	v_mov_b32_e32 v7, v9
	v_pk_mul_f32 v[6:7], v[6:7], v[116:117]
	s_nop 0
	v_sub_f32_e32 v15, v6, v7
	v_mov_b32_e32 v6, v8
	v_mov_b32_e32 v7, v16
	v_pk_mul_f32 v[6:7], v[6:7], v[114:115]
	v_mov_b32_e32 v16, v9
	v_add_f32_e32 v8, v6, v7
	v_pk_mul_f32 v[6:7], v[16:17], v[116:117]
	s_waitcnt vmcnt(4)
	v_mov_b32_e32 v9, v84
	v_add_f32_e32 v6, v6, v7
	v_cvt_pk_bf16_f32 v109, v8, v6
	v_pk_mul_f32 v[6:7], v[18:19], v[72:73] op_sel_hi:[0,1]
	v_mov_b32_e32 v8, v76
	v_pk_mul_f32 v[28:29], v[6:7], v[8:9]
	v_pk_mul_f32 v[6:7], v[18:19], v[70:71] op_sel_hi:[0,1]
	v_mov_b32_e32 v84, v77
	v_pk_mul_f32 v[70:71], v[6:7], v[84:85]
	v_pk_mul_f32 v[6:7], v[18:19], v[68:69] op_sel_hi:[0,1]
	v_mov_b32_e32 v8, v78
	v_mov_b32_e32 v9, v86
	v_pk_mul_f32 v[72:73], v[6:7], v[8:9]
	v_pk_mul_f32 v[6:7], v[18:19], v[66:67] op_sel_hi:[0,1]
	v_mov_b32_e32 v86, v79
	v_pk_mul_f32 v[74:75], v[6:7], v[86:87]
	v_pk_mul_f32 v[6:7], v[18:19], v[64:65] op_sel_hi:[0,1]
	v_mov_b32_e32 v8, v10
	v_mov_b32_e32 v9, v80
	v_pk_mul_f32 v[76:77], v[6:7], v[8:9]
	v_pk_mul_f32 v[6:7], v[18:19], v[62:63] op_sel_hi:[0,1]
	v_mov_b32_e32 v80, v11
	v_pk_mul_f32 v[10:11], v[18:19], v[60:61] op_sel_hi:[0,1]
	v_mov_b32_e32 v64, v12
	v_mov_b32_e32 v65, v82
	v_cvt_pk_bf16_f32 v113, v14, v15
	v_pk_mul_f32 v[78:79], v[6:7], v[80:81]
	global_load_dwordx4 v[6:9], v44, s[14:15] offset:336
	global_load_dwordx4 v[14:17], v44, s[14:15] offset:320
	global_load_dwordx4 v[24:27], v44, s[14:15] offset:464
	global_load_dwordx4 v[60:63], v44, s[14:15] offset:448
	v_pk_mul_f32 v[44:45], v[10:11], v[64:65]
	v_pk_mul_f32 v[10:11], v[18:19], v[54:55] op_sel_hi:[0,1]
	v_mov_b32_e32 v82, v13
	v_pk_mul_f32 v[80:81], v[10:11], v[82:83]
	s_waitcnt vmcnt(6)
	v_mov_b32_e32 v54, v88
	s_waitcnt vmcnt(5)
	v_mov_b32_e32 v55, v92
	v_pk_mul_f32 v[54:55], v[54:55], v[28:29]
	global_load_dwordx4 v[10:13], v[118:119], off offset:64
	v_sub_f32_e32 v19, v54, v55
	v_mov_b32_e32 v54, v89
	v_mov_b32_e32 v55, v93
	v_pk_mul_f32 v[54:55], v[54:55], v[70:71]
	s_nop 0
	v_sub_f32_e32 v31, v54, v55
	v_mov_b32_e32 v54, v92
	v_mov_b32_e32 v55, v88
	v_pk_mul_f32 v[28:29], v[54:55], v[28:29]
	v_mov_b32_e32 v88, v93
	v_add_f32_e32 v33, v28, v29
	v_pk_mul_f32 v[28:29], v[88:89], v[70:71]
	global_load_dwordx4 v[64:67], v[58:59], off offset:80
	global_load_dwordx4 v[68:71], v[58:59], off offset:64
	v_add_f32_e32 v28, v28, v29
	global_load_dwordx4 v[54:57], v[56:57], off offset:16
	v_cvt_pk_bf16_f32 v114, v33, v28
	v_mov_b32_e32 v28, v90
	v_mov_b32_e32 v29, v94
	v_pk_mul_f32 v[28:29], v[28:29], v[72:73]
	v_cvt_pk_bf16_f32 v118, v19, v31
	s_nop 0
	v_sub_f32_e32 v19, v28, v29
	v_mov_b32_e32 v28, v91
	v_mov_b32_e32 v29, v95
	v_pk_mul_f32 v[28:29], v[28:29], v[74:75]
	s_nop 0
	v_sub_f32_e32 v31, v28, v29
	v_mov_b32_e32 v28, v94
	v_mov_b32_e32 v29, v90
	v_pk_mul_f32 v[28:29], v[28:29], v[72:73]
	v_mov_b32_e32 v90, v95
	v_add_f32_e32 v33, v28, v29
	v_pk_mul_f32 v[28:29], v[90:91], v[74:75]
	v_cvt_pk_bf16_f32 v119, v19, v31
	s_nop 0
	v_add_f32_e32 v28, v28, v29
	v_cvt_pk_bf16_f32 v115, v33, v28
	v_mov_b32_e32 v28, v2
	s_waitcnt vmcnt(8)
	v_mov_b32_e32 v29, v20
	v_pk_mul_f32 v[28:29], v[28:29], v[76:77]
	s_nop 0
	v_sub_f32_e32 v19, v28, v29
	v_mov_b32_e32 v28, v3
	v_mov_b32_e32 v29, v21
	v_pk_mul_f32 v[28:29], v[28:29], v[78:79]
	s_nop 0
	v_sub_f32_e32 v31, v28, v29
	v_mov_b32_e32 v29, v2
	v_mov_b32_e32 v2, v21
	v_mov_b32_e32 v28, v20
	v_pk_mul_f32 v[2:3], v[2:3], v[78:79]
	v_pk_mul_f32 v[28:29], v[28:29], v[76:77]
	v_add_f32_e32 v2, v2, v3
	v_add_f32_e32 v20, v28, v29
	v_cvt_pk_bf16_f32 v116, v20, v2
	v_mov_b32_e32 v2, v4
	v_mov_b32_e32 v3, v22
	v_pk_mul_f32 v[2:3], v[2:3], v[44:45]
	v_cvt_pk_bf16_f32 v120, v19, v31
	s_nop 0
	v_sub_f32_e32 v19, v2, v3
	v_mov_b32_e32 v2, v5
	v_mov_b32_e32 v3, v23
	v_pk_mul_f32 v[2:3], v[2:3], v[80:81]
	s_nop 0
	v_sub_f32_e32 v20, v2, v3
	v_mov_b32_e32 v2, v22
	v_mov_b32_e32 v3, v4
	v_pk_mul_f32 v[2:3], v[2:3], v[44:45]
	v_mov_b32_e32 v4, v23
	v_add_f32_e32 v21, v2, v3
	v_pk_mul_f32 v[2:3], v[4:5], v[80:81]
	v_cvt_pk_bf16_f32 v121, v19, v20
	s_waitcnt vmcnt(6)
; __device__ __forceinline__ unsigned pk2(float lo, float hi) { unsigned r; asm("v_cvt_pk_bf16_f32 %0, %1, %2" : "=v"(r) : "v"(lo), "v"(hi)); return r; }
; __device__ __forceinline__ int v_rd_base(int lane) { return ((lane & 3) << 3) | (((lane >> 2) & 3) << 6) | (((lane >> 4) & 1) << 5) | (((lane >> 5) & 1) << 8); }
; #define ATT_WAIT_BAR() asm volatile("s_waitcnt vmcnt(0) lgkmcnt(0)\n\ts_barrier" ::: "memory")
; __device__ __forceinline__ void qkt(f32x16& p0, f32x16& p1, const bf16_t* Ks, const bf16x8* qr, int r32, int hi) {
;   p0 = f32x16{}; p1 = f32x16{};
;   for (int d0 = 0; d0 < 8; ++d0) { int cb = (d0 * 16 + hi * 8) * 2;
;     bf16x8 b0 = *reinterpret_cast<const bf16x8*>((const char*)Ks + KSWZ(r32, cb));
;     bf16x8 b1 = *reinterpret_cast<const bf16x8*>((const char*)Ks + KSWZ(32 + r32, cb));
;     p0 = __builtin_amdgcn_mfma_f32_32x32x16_bf16(b0, qr[d0], p0, 0, 0, 0);
;     p1 = __builtin_amdgcn_mfma_f32_32x32x16_bf16(b1, qr[d0], p1, 0, 0, 0); }
; __device__ __forceinline__ void attn_dma_body(const bf16_t* __restrict__ Qb, int ldq, int tpos0, const float* __restrict__ rope, const float* __restrict__ qgain, ...
;     ...
;         for (int i = 0; i < 4; ++i) { const float l0 = lo[2 * i] * cs[2 * i] - hv[2 * i] * sn[2 * i], l1 = lo[2 * i + 1] * cs[2 * i + 1] - hv[2 * i + 1] * sn[2 * i + 1];
;           const float h0 = hv[2 * i] * cs[2 * i] + lo[2 * i] * sn[2 * i], h1 = hv[2 * i + 1] * cs[2 * i + 1] + lo[2 * i + 1] * sn[2 * i + 1];
;           wl[i] = pk2(l0, l1); wh[i] = pk2(h0, h1); }
;         qr[dl] = *reinterpret_cast<bf16x8*>(&wl); qr[dh] = *reinterpret_cast<bf16x8*>(&wh); } } }
; #pragma unroll
;   for (int d0 = 0; d0 < 8; ++d0) asm volatile("" : "+v"(qr[d0]));
;   ATT_WAIT_BAR();
;   if (2 < NT) ATT_DMA(2, 2);
;   const int vb0 = (int)(uintptr_t)lds + 16384 + v_rd_base(lane);
;   f32x16 pA0, pA1, pB0, pB1; float mnA, mnB, alA, alB; bf16x8 pa0, pa1, pa2, pa3;
;   qkt(pA0, pA1, (const bf16_t*)lds, qr, r32, hi); partialSM(pA0, pA1, m_reg, mnA, alA);
	v_mov_b32_e32 v4, v14
	v_add_f32_e32 v2, v2, v3
	v_cvt_pk_bf16_f32 v117, v21, v2
	s_waitcnt vmcnt(4)
	v_mov_b32_e32 v5, v60
	v_mov_b32_e32 v60, v15
	v_pk_mul_f32 v[14:15], v[18:19], v[48:49] op_sel_hi:[0,1]
	v_mov_b32_e32 v20, v16
	v_mov_b32_e32 v21, v62
	v_pk_mul_f32 v[14:15], v[14:15], v[20:21]
	v_pk_mul_f32 v[20:21], v[18:19], v[46:47] op_sel_hi:[0,1]
	v_mov_b32_e32 v62, v17
	v_pk_mul_f32 v[16:17], v[20:21], v[62:63]
	v_pk_mul_f32 v[20:21], v[18:19], v[42:43] op_sel_hi:[0,1]
	v_mov_b32_e32 v22, v6
	v_mov_b32_e32 v23, v24
	v_pk_mul_f32 v[2:3], v[18:19], v[52:53] op_sel_hi:[0,1]
	v_pk_mul_f32 v[20:21], v[20:21], v[22:23]
	v_pk_mul_f32 v[22:23], v[18:19], v[40:41] op_sel_hi:[0,1]
	v_mov_b32_e32 v24, v7
	v_pk_mul_f32 v[2:3], v[2:3], v[4:5]
	v_pk_mul_f32 v[4:5], v[18:19], v[50:51] op_sel_hi:[0,1]
	v_pk_mul_f32 v[6:7], v[22:23], v[24:25]
	v_pk_mul_f32 v[22:23], v[18:19], v[38:39] op_sel_hi:[0,1]
	v_mov_b32_e32 v25, v26
	v_pk_mul_f32 v[18:19], v[18:19], v[36:37] op_sel_hi:[0,1]
	v_mov_b32_e32 v26, v9
	v_mov_b32_e32 v24, v8
	v_pk_mul_f32 v[8:9], v[18:19], v[26:27]
	s_waitcnt vmcnt(1)
	v_mov_b32_e32 v18, v68
	v_mov_b32_e32 v19, v10
	v_pk_mul_f32 v[18:19], v[18:19], v[2:3]
	v_pk_mul_f32 v[4:5], v[4:5], v[60:61]
	v_pk_mul_f32 v[22:23], v[22:23], v[24:25]
	v_sub_f32_e32 v24, v18, v19
	v_mov_b32_e32 v18, v69
	v_mov_b32_e32 v19, v11
	v_pk_mul_f32 v[18:19], v[18:19], v[4:5]
	s_nop 0
	v_sub_f32_e32 v25, v18, v19
	v_mov_b32_e32 v18, v10
	v_mov_b32_e32 v19, v68
	v_pk_mul_f32 v[2:3], v[18:19], v[2:3]
	v_mov_b32_e32 v68, v11
	v_add_f32_e32 v10, v2, v3
	v_pk_mul_f32 v[2:3], v[68:69], v[4:5]
	v_cvt_pk_bf16_f32 v126, v24, v25
	s_nop 0
	v_add_f32_e32 v2, v2, v3
	v_cvt_pk_bf16_f32 v122, v10, v2
	v_mov_b32_e32 v2, v70
	v_mov_b32_e32 v3, v12
	v_pk_mul_f32 v[2:3], v[2:3], v[14:15]
	s_nop 0
	v_sub_f32_e32 v4, v2, v3
	v_mov_b32_e32 v2, v71
	v_mov_b32_e32 v3, v13
	v_pk_mul_f32 v[2:3], v[2:3], v[16:17]
	s_nop 0
	v_sub_f32_e32 v5, v2, v3
	v_mov_b32_e32 v2, v12
	v_mov_b32_e32 v3, v70
	v_pk_mul_f32 v[2:3], v[2:3], v[14:15]
	v_mov_b32_e32 v70, v13
	v_add_f32_e32 v10, v2, v3
	v_pk_mul_f32 v[2:3], v[70:71], v[16:17]
	v_cvt_pk_bf16_f32 v127, v4, v5
	s_nop 0
	v_add_f32_e32 v2, v2, v3
	v_cvt_pk_bf16_f32 v123, v10, v2
	v_mov_b32_e32 v2, v64
	s_waitcnt vmcnt(0)
	v_mov_b32_e32 v3, v54
	v_pk_mul_f32 v[2:3], v[2:3], v[20:21]
	s_nop 0
	v_sub_f32_e32 v4, v2, v3
	v_mov_b32_e32 v2, v65
	v_mov_b32_e32 v3, v55
	v_pk_mul_f32 v[2:3], v[2:3], v[6:7]
	s_nop 0
	v_sub_f32_e32 v5, v2, v3
	v_mov_b32_e32 v2, v54
	v_mov_b32_e32 v3, v64
	v_pk_mul_f32 v[2:3], v[2:3], v[20:21]
	v_mov_b32_e32 v64, v55
	v_add_f32_e32 v10, v2, v3
	v_pk_mul_f32 v[2:3], v[64:65], v[6:7]
	v_cvt_pk_bf16_f32 v128, v4, v5
	s_nop 0
	v_add_f32_e32 v2, v2, v3
	v_cvt_pk_bf16_f32 v124, v10, v2
	v_mov_b32_e32 v2, v66
	v_mov_b32_e32 v3, v56
	v_pk_mul_f32 v[2:3], v[2:3], v[22:23]
	s_nop 0
	v_sub_f32_e32 v4, v2, v3
	v_mov_b32_e32 v2, v67
	v_mov_b32_e32 v3, v57
	v_pk_mul_f32 v[2:3], v[2:3], v[8:9]
	s_nop 0
	v_sub_f32_e32 v5, v2, v3
	v_mov_b32_e32 v2, v56
	v_mov_b32_e32 v3, v66
	v_pk_mul_f32 v[2:3], v[2:3], v[22:23]
	v_mov_b32_e32 v66, v57
	v_add_f32_e32 v6, v2, v3
	v_pk_mul_f32 v[2:3], v[66:67], v[8:9]
	v_cvt_pk_bf16_f32 v129, v4, v5
	s_nop 0
	v_add_f32_e32 v2, v2, v3
	v_cvt_pk_bf16_f32 v125, v6, v2
.LBB0_408:
	s_add_u32 s2, s38, 0x8000
	s_addc_u32 s3, s39, 0
	s_add_u32 s4, s40, 0x8000
	v_mov_b32_e32 v31, v163
	s_waitcnt vmcnt(0)
	s_waitcnt vmcnt(0) lgkmcnt(0)
	s_barrier
	s_addc_u32 s5, s41, 0
	s_add_i32 m0, s96, 0x10000
	s_add_i32 s6, s96, 0x14000
	v_lshl_add_u64 v[2:3], s[2:3], 0, v[162:163]
	v_mov_b32_e32 v33, v163
	global_load_lds_dwordx4 v[2:3], off
	v_lshl_add_u64 v[2:3], s[4:5], 0, v[30:31]
	s_mov_b32 m0, s6
	v_mov_b32_e32 v35, v163
	global_load_lds_dwordx4 v[2:3], off
	v_lshl_add_u64 v[2:3], s[2:3], 0, v[32:33]
	s_add_i32 m0, s96, 0x12000
	v_lshlrev_b32_e32 v10, 8, v177
	global_load_lds_dwordx4 v[2:3], off
	v_lshl_add_u64 v[2:3], s[4:5], 0, v[34:35]
	s_add_i32 m0, s96, 0x16000
	v_and_b32_e32 v167, 63, v147
	global_load_lds_dwordx4 v[2:3], off
	v_lshlrev_b32_e32 v2, 4, v177
	v_and_b32_e32 v11, 0x70, v2
	v_bitop3_b32 v183, v166, v10, v11 bitop3:0xde
	v_add_u32_e32 v6, 0, v183
	ds_read_b128 v[2:5], v6
	ds_read_b128 v[6:9], v6 offset:8192
	s_waitcnt lgkmcnt(0)
	v_mfma_f32_32x32x16_bf16 v[18:33], v[2:5], v[102:105], 0
	v_or_b32_e32 v2, 32, v166
	v_bitop3_b32 v184, v2, v10, v11 bitop3:0xde
	v_and_b32_e32 v12, 0x3fffffc0, v147
	v_lshl_add_u32 v165, v12, 2, s90
	v_lshlrev_b32_e32 v12, 3, v167
	s_cmp_lg_u32 0, -1
	s_cselect_b32 s2, 0, 0
	v_mfma_f32_32x32x16_bf16 v[34:49], v[6:9], v[102:105], 0
	v_add_u32_e32 v6, 0, v184
	ds_read_b128 v[2:5], v6
	ds_read_b128 v[6:9], v6 offset:8192
	s_addk_i32 s2, 0x4000
	s_mov_b32 s72, s73
	s_mov_b32 s74, s73
	s_mov_b32 s75, s73
	s_mov_b32 s76, s73
	s_waitcnt lgkmcnt(0)
	v_mfma_f32_32x32x16_bf16 v[18:33], v[2:5], v[110:113], v[18:33]
	v_or_b32_e32 v2, 64, v166
	v_bitop3_b32 v186, v2, v10, v11 bitop3:0xde
	s_mov_b32 s77, s73
	s_mov_b32 s78, s73
	s_mov_b32 s79, s73
	s_mov_b32 s80, s73
	s_mov_b32 s81, s73
	v_mfma_f32_32x32x16_bf16 v[34:49], v[6:9], v[110:113], v[34:49]
	v_add_u32_e32 v6, 0, v186
	ds_read_b128 v[2:5], v6
	ds_read_b128 v[6:9], v6 offset:8192
	s_mov_b32 s82, s73
	s_mov_b32 s83, s73
	s_mov_b32 s84, s73
	s_mov_b32 s85, s73
	s_mov_b32 s86, s73
	s_waitcnt lgkmcnt(0)
	v_mfma_f32_32x32x16_bf16 v[18:33], v[2:5], v[98:101], v[18:33]
	v_or_b32_e32 v2, 0x60, v166
	v_bitop3_b32 v185, v2, v10, v11 bitop3:0xde
	s_mov_b32 s87, s73
	s_mov_b32 s36, 0x10000
	s_mov_b32 s97, -1
	v_lshl_add_u32 v180, v177, 2, v165
	v_mov_b32_e32 v169, v163
	v_mfma_f32_32x32x16_bf16 v[34:49], v[6:9], v[98:101], v[34:49]
	v_add_u32_e32 v6, 0, v185
	ds_read_b128 v[2:5], v6
	ds_read_b128 v[6:9], v6 offset:8192
	v_add_u32_e32 v170, v149, v150
	v_mov_b32_e32 v171, v163
	v_add_u32_e32 v172, v151, v152
	v_mov_b32_e32 v173, v163
	v_mov_b32_e32 v182, 0
	s_waitcnt lgkmcnt(0)
; __device__ __forceinline__ void partialSM(f32x16& p0, f32x16& p1, float& m_reg, float& mn, float& alpha) {
;   constexpr float C = SCALE * 1.4426950408889634f;
;   float pmax = p0[0]; for (int r = 1; r < 16; ++r) pmax = fmaxf(pmax, p0[r]); for (int r = 0; r < 16; ++r) pmax = fmaxf(pmax, p1[r]);
;   { auto rr = __builtin_amdgcn_permlane32_swap(__float_as_uint(pmax), __float_as_uint(pmax), false, false);
;     pmax = fmaxf(__uint_as_float(rr[0]), __uint_as_float(rr[1])); }
;   if (__builtin_expect(__all(pmax - m_reg <= THR / SCALE), 1)) { mn = m_reg; alpha = 1.f; }
;   else { mn = fmaxf(m_reg, pmax); alpha = __builtin_amdgcn_exp2f((m_reg - mn) * C); m_reg = mn; }
;   float mnC = -mn * C;
;   for (int r = 0; r < 16; ++r) p0[r] = fmaf(p0[r], C, mnC); for (int r = 0; r < 16; ++r) p1[r] = fmaf(p1[r], C, mnC);
;   for (int r = 0; r < 16; ++r) p0[r] = __builtin_amdgcn_exp2f(p0[r]);
; }
; __device__ __forceinline__ void qkt(f32x16& p0, f32x16& p1, const bf16_t* Ks, const bf16x8* qr, int r32, int hi) {
;   p0 = f32x16{}; p1 = f32x16{};
;   for (int d0 = 0; d0 < 8; ++d0) { int cb = (d0 * 16 + hi * 8) * 2;
;     bf16x8 b0 = *reinterpret_cast<const bf16x8*>((const char*)Ks + KSWZ(r32, cb));
;     bf16x8 b1 = *reinterpret_cast<const bf16x8*>((const char*)Ks + KSWZ(32 + r32, cb));
;     p0 = __builtin_amdgcn_mfma_f32_32x32x16_bf16(b0, qr[d0], p0, 0, 0, 0);
;     p1 = __builtin_amdgcn_mfma_f32_32x32x16_bf16(b1, qr[d0], p1, 0, 0, 0); }
	v_mfma_f32_32x32x16_bf16 v[18:33], v[2:5], v[106:109], v[18:33]
	v_or_b32_e32 v2, 0x80, v166
	v_bitop3_b32 v187, v2, v10, v11 bitop3:0xde
	v_mfma_f32_32x32x16_bf16 v[34:49], v[6:9], v[106:109], v[34:49]
	v_add_u32_e32 v6, 0, v187
	ds_read_b128 v[2:5], v6
	ds_read_b128 v[6:9], v6 offset:8192
	s_waitcnt lgkmcnt(0)
	v_mfma_f32_32x32x16_bf16 v[18:33], v[2:5], v[118:121], v[18:33]
	v_or_b32_e32 v2, 0xa0, v166
	v_bitop3_b32 v188, v2, v10, v11 bitop3:0xde
	v_add_u32_e32 v13, 0, v188
	ds_read_b128 v[2:5], v13
	v_mfma_f32_32x32x16_bf16 v[34:49], v[6:9], v[118:121], v[34:49]
	v_lshlrev_b32_e32 v6, 4, v167
	v_and_b32_e32 v6, 0xc0, v6
	v_and_or_b32 v14, v12, 24, v6
	v_lshlrev_b32_e32 v6, 1, v167
	v_and_b32_e32 v15, 32, v6
	v_and_b32_e32 v12, 0x100, v12
	v_or3_b32 v181, v14, v15, v12
	s_waitcnt lgkmcnt(0)
	v_mfma_f32_32x32x16_bf16 v[18:33], v[2:5], v[126:129], v[18:33]
	v_or_b32_e32 v2, 0xc0, v166
	v_bitop3_b32 v189, v2, v10, v11 bitop3:0xde
	v_add_u32_e32 v12, 0, v189
	ds_read_b128 v[6:9], v13 offset:8192
	ds_read_b128 v[2:5], v12
	v_add_u32_e32 v191, s2, v181
	v_readfirstlane_b32 s2, v179
	s_waitcnt lgkmcnt(0)
	v_mfma_f32_32x32x16_bf16 v[34:49], v[6:9], v[126:129], v[34:49]
	ds_read_b128 v[6:9], v12 offset:8192
	s_cmp_lt_i32 s2, 4
	s_cselect_b64 s[34:35], -1, 0
	s_cmp_gt_i32 s2, 3
	s_cselect_b64 s[38:39], -1, 0
	v_cmp_gt_u32_e64 s[2:3], 32, v167
	v_mfma_f32_32x32x16_bf16 v[18:33], v[2:5], v[114:117], v[18:33]
	v_or_b32_e32 v2, 0xe0, v166
	v_bitop3_b32 v190, v2, v10, v11 bitop3:0xde
	v_add_u32_e32 v10, 0, v190
	ds_read_b128 v[2:5], v10
	ds_read_b128 v[50:53], v10 offset:8192
	s_waitcnt lgkmcnt(0)
	v_mfma_f32_32x32x16_bf16 v[18:33], v[2:5], v[122:125], v[18:33]
	v_mfma_f32_32x32x16_bf16 v[34:49], v[6:9], v[114:117], v[34:49]
	s_nop 10
	v_max_f32_e32 v54, v19, v19
	v_max_f32_e32 v55, v18, v18
	v_max_f32_e32 v54, v55, v54
	v_mov_b64_e32 v[2:3], s[72:73]
	v_mov_b64_e32 v[16:17], s[86:87]
	v_mov_b64_e32 v[4:5], s[74:75]
	v_mov_b64_e32 v[6:7], s[76:77]
	v_mfma_f32_32x32x16_bf16 v[34:49], v[50:53], v[122:125], v[34:49]
	v_max3_f32 v50, v54, v20, v21
	v_max3_f32 v50, v50, v22, v23
	v_max3_f32 v50, v50, v24, v25
	v_max3_f32 v50, v50, v26, v27
	v_max3_f32 v50, v50, v28, v29
	v_max3_f32 v50, v50, v30, v31
	v_max3_f32 v50, v50, v32, v33
	s_nop 4
	v_max3_f32 v50, v50, v34, v35
	v_max3_f32 v50, v50, v36, v37
	v_max3_f32 v50, v50, v38, v39
	v_max3_f32 v50, v50, v40, v41
	v_max3_f32 v50, v50, v42, v43
	v_max3_f32 v50, v50, v44, v45
	v_max3_f32 v50, v50, v46, v47
	v_max3_f32 v50, v50, v48, v49
	v_mov_b32_e32 v51, v50
	s_nop 1
	v_permlane32_swap_b32_e32 v50, v51
	v_max_f32_e32 v51, v51, v51
	v_max_f32_e32 v50, v50, v50
	v_max_f32_e32 v50, v50, v51
	v_add_f32_e32 v51, 0x7149f2ca, v50
	v_cmp_ge_f32_e32 vcc, s89, v51
	s_cmp_eq_u64 vcc, exec
	v_max_f32_e32 v50, 0xf149f2ca, v50
	s_cselect_b64 vcc, -1, 0
	v_cndmask_b32_e32 v193, v50, v175, vcc
	v_sub_f32_e32 v51, 0xf149f2ca, v50
	v_mul_f32_e32 v50, 0xbe0293ee, v193
	v_fmamk_f32 v18, v18, 0x3e0293ee, v50
	v_exp_f32_e32 v203, v18
	v_fmamk_f32 v18, v19, 0x3e0293ee, v50
	v_exp_f32_e32 v207, v18
	v_fmamk_f32 v18, v20, 0x3e0293ee, v50
	v_exp_f32_e32 v204, v18
	v_fmamk_f32 v18, v21, 0x3e0293ee, v50
	v_exp_f32_e32 v208, v18
	v_fmamk_f32 v18, v22, 0x3e0293ee, v50
	v_exp_f32_e32 v205, v18
	v_fmamk_f32 v18, v23, 0x3e0293ee, v50
	v_exp_f32_e32 v209, v18
	v_fmamk_f32 v18, v24, 0x3e0293ee, v50
	v_exp_f32_e32 v202, v18
	v_fmamk_f32 v18, v25, 0x3e0293ee, v50
	v_exp_f32_e32 v206, v18
	v_fmamk_f32 v18, v26, 0x3e0293ee, v50
	v_exp_f32_e32 v159, v18
	v_fmamk_f32 v18, v27, 0x3e0293ee, v50
	v_exp_f32_e32 v199, v18
	v_fmamk_f32 v18, v28, 0x3e0293ee, v50
	v_mul_f32_e32 v51, 0x3e0293ee, v51
	v_exp_f32_e32 v160, v18
	v_fmamk_f32 v18, v29, 0x3e0293ee, v50
	v_exp_f32_e32 v51, v51
	v_exp_f32_e32 v200, v18
	v_fmamk_f32 v18, v30, 0x3e0293ee, v50
	v_exp_f32_e32 v157, v18
	v_fmamk_f32 v18, v31, 0x3e0293ee, v50
	v_exp_f32_e32 v161, v18
	v_fmamk_f32 v18, v32, 0x3e0293ee, v50
	v_exp_f32_e32 v158, v18
	v_add3_u32 v18, v154, v148, v156
	v_lshlrev_b32_e32 v19, 1, v147
	v_lshlrev_b32_e32 v20, 4, v147
	v_pk_fma_f32 v[130:131], v[48:49], s[20:21], v[50:51] op_sel_hi:[1,0,0]
	v_pk_fma_f32 v[132:133], v[46:47], s[20:21], v[50:51] op_sel_hi:[1,0,0]
	v_pk_fma_f32 v[134:135], v[44:45], s[20:21], v[50:51] op_sel_hi:[1,0,0]
	v_pk_fma_f32 v[136:137], v[42:43], s[20:21], v[50:51] op_sel_hi:[1,0,0]
	v_pk_fma_f32 v[138:139], v[40:41], s[20:21], v[50:51] op_sel_hi:[1,0,0]
	v_pk_fma_f32 v[140:141], v[38:39], s[20:21], v[50:51] op_sel_hi:[1,0,0]
	v_pk_fma_f32 v[142:143], v[36:37], s[20:21], v[50:51] op_sel_hi:[1,0,0]
	v_pk_fma_f32 v[144:145], v[34:35], s[20:21], v[50:51] op_sel_hi:[1,0,0]
	v_fmac_f32_e32 v50, 0x3e0293ee, v33
	v_add_lshl_u32 v18, v18, v146, 8
	v_and_b32_e32 v19, 0xc0, v19
	v_and_b32_e32 v20, 48, v20
	v_exp_f32_e32 v201, v50
	v_or3_b32 v162, v18, v19, v20
	v_add3_u32 v18, v153, v148, v155
	v_add_lshl_u32 v18, v18, v146, 8
	v_mov_b64_e32 v[8:9], s[78:79]
	v_mov_b64_e32 v[10:11], s[80:81]
	v_mov_b64_e32 v[12:13], s[82:83]
	v_mov_b64_e32 v[14:15], s[84:85]
	v_cndmask_b32_e64 v192, v51, 1.0, vcc
	s_add_u32 s40, s28, s69
	v_or3_b32 v168, v18, v19, v20
	v_mov_b64_e32 v[64:65], v[16:17]
	v_mov_b64_e32 v[48:49], v[16:17]
	v_mov_b64_e32 v[32:33], v[16:17]
	s_addc_u32 s41, s29, s65
	v_mov_b64_e32 v[62:63], v[14:15]
	v_mov_b64_e32 v[60:61], v[12:13]
	v_mov_b64_e32 v[58:59], v[10:11]
	v_mov_b64_e32 v[56:57], v[8:9]
	v_mov_b64_e32 v[54:55], v[6:7]
	v_mov_b64_e32 v[52:53], v[4:5]
	v_mov_b64_e32 v[50:51], v[2:3]
	v_mov_b64_e32 v[46:47], v[14:15]
	v_mov_b64_e32 v[44:45], v[12:13]
	v_mov_b64_e32 v[42:43], v[10:11]
	v_mov_b64_e32 v[40:41], v[8:9]
	v_mov_b64_e32 v[38:39], v[6:7]
	v_mov_b64_e32 v[36:37], v[4:5]
	v_mov_b64_e32 v[34:35], v[2:3]
	v_mov_b64_e32 v[30:31], v[14:15]
	v_mov_b64_e32 v[28:29], v[12:13]
	v_mov_b64_e32 v[26:27], v[10:11]
	v_mov_b64_e32 v[24:25], v[8:9]
	v_mov_b64_e32 v[22:23], v[6:7]
	v_mov_b64_e32 v[20:21], v[4:5]
	v_mov_b64_e32 v[18:19], v[2:3]
; #define SBAR() __builtin_amdgcn_sched_barrier(0)
; #define ATT_SYNC(jn) do { ATT_WAIT_BAR(); if ((jn) < NT) ATT_DMA((jn), (jn) & 3); } while (0)
; __device__ __forceinline__ void finishSM(f32x16& p0, f32x16& p1, float alpha, float& l_reg, bf16x8& pa0, bf16x8& pa1, bf16x8& pa2, bf16x8& pa3) {
;   for (int r = 0; r < 16; ++r) p1[r] = __builtin_amdgcn_exp2f(p1[r]);
;   float ps = 0; for (int r = 0; r < 16; ++r) ps += p0[r]; for (int r = 0; r < 16; ++r) ps += p1[r];
;   { auto rr = __builtin_amdgcn_permlane32_swap(__float_as_uint(ps), __float_as_uint(ps), false, false);
;     ps = __uint_as_float(rr[0]) + __uint_as_float(rr[1]); }
;   l_reg = l_reg * alpha + ps;
;     ...
;   PK4(p0, 0, pa0); PK4(p0, 8, pa1); PK4(p1, 0, pa2); PK4(p1, 8, pa3);
;     ...
; }
; __device__ __forceinline__ void attn_dma_body(const bf16_t* __restrict__ Qb, int ldq, int tpos0, const float* __restrict__ rope, const float* __restrict__ qgain, ...
;     ...
;   for (int j = 1; j + 1 < NT; j += 2) {
;     { SBAR(); qkt(pB0, pB1, (const bf16_t*)(lds + (j & 3) * SHM_SLOT), qr, r32, hi);
;       finishSM(pA0, pA1, alA, l_reg, pa0, pa1, pa2, pa3); s16x4 va[8]; pv_rd<0>(va, vb0 + ((j - 1) & 3) * (int)SHM_SLOT); SBAR();
;       if (!lead) ATT_SYNC(j + 2);
.LBB0_409:
	s_add_i32 s4, s36, 0xffff8000
	s_and_b32 s69, s4, 0x18000
	s_add_i32 s4, s69, 0
	v_add_u32_e32 v70, s4, v183
	ds_read_b128 v[66:69], v70
	ds_read_b128 v[70:73], v70 offset:8192
	v_add_u32_e32 v154, s4, v186
	v_add_u32_e32 v155, s4, v185
	v_add_u32_e32 v156, s4, v187
	s_waitcnt lgkmcnt(0)
	v_mfma_f32_32x32x16_bf16 v[82:97], v[66:69], v[102:105], 0
	v_add_u32_e32 v66, s4, v184
	ds_read_b128 v[146:149], v66
	ds_read_b128 v[150:153], v66 offset:8192
	ds_read_b128 v[194:197], v154
	ds_read_b128 v[210:213], v154 offset:8192
	ds_read_b128 v[214:217], v155
	ds_read_b128 v[218:221], v155 offset:8192
	ds_read_b128 v[222:225], v156
	ds_read_b128 v[226:229], v156 offset:8192
	v_add_u32_e32 v154, s4, v188
	v_exp_f32_e32 v144, v144
	v_exp_f32_e32 v145, v145
	v_exp_f32_e32 v142, v142
	v_mfma_f32_32x32x16_bf16 v[66:81], v[70:73], v[102:105], 0
	v_exp_f32_e32 v143, v143
	v_exp_f32_e32 v140, v140
	v_exp_f32_e32 v141, v141
	v_exp_f32_e32 v155, v139
	v_exp_f32_e32 v156, v136
	v_exp_f32_e32 v198, v135
	v_exp_f32_e32 v246, v132
	s_waitcnt lgkmcnt(0)
	v_mfma_f32_32x32x16_bf16 v[82:97], v[146:149], v[110:113], v[82:97]
	ds_read_b128 v[146:149], v154
	ds_read_b128 v[230:233], v154 offset:8192
	v_add_u32_e32 v154, s4, v189
	ds_read_b128 v[234:237], v154
	ds_read_b128 v[238:241], v154 offset:8192
	v_add_u32_e32 v154, s4, v190
	s_add_i32 s37, s36, 0x10000
	s_and_b32 s65, s37, 0x18000
	v_mfma_f32_32x32x16_bf16 v[66:81], v[150:153], v[110:113], v[66:81]
	ds_read_b128 v[150:153], v154
	ds_read_b128 v[242:245], v154 offset:8192
	v_exp_f32_e32 v154, v138
	v_mfma_f32_32x32x16_bf16 v[82:97], v[194:197], v[98:101], v[82:97]
	v_exp_f32_e32 v196, v137
	v_exp_f32_e32 v197, v134
	v_mfma_f32_32x32x16_bf16 v[66:81], v[210:213], v[98:101], v[66:81]
	v_exp_f32_e32 v211, v130
	v_add_f32_e32 v130, v207, v203
	v_add_f32_e32 v130, v204, v130
	v_add_f32_e32 v130, v208, v130
	v_add_f32_e32 v130, v205, v130
	v_add_f32_e32 v130, v209, v130
	v_mfma_f32_32x32x16_bf16 v[82:97], v[214:217], v[106:109], v[82:97]
	v_add_f32_e32 v130, v202, v130
	v_add_f32_e32 v130, v206, v130
	v_add_f32_e32 v130, v159, v130
	v_add_f32_e32 v130, v199, v130
	v_add_f32_e32 v130, v160, v130
	v_add_f32_e32 v130, v200, v130
	v_add_f32_e32 v130, v157, v130
	v_mfma_f32_32x32x16_bf16 v[66:81], v[218:221], v[106:109], v[66:81]
	v_add_f32_e32 v130, v161, v130
	v_add_f32_e32 v130, v158, v130
	v_add_f32_e32 v130, v201, v130
	v_add_f32_e32 v130, v144, v130
	v_add_f32_e32 v130, v145, v130
	v_add_f32_e32 v130, v142, v130
	v_add_f32_e32 v130, v143, v130
	v_mfma_f32_32x32x16_bf16 v[82:97], v[222:225], v[118:121], v[82:97]
	v_add_f32_e32 v130, v140, v130
	v_add_f32_e32 v130, v141, v130
	v_add_f32_e32 v130, v154, v130
	v_add_f32_e32 v130, v155, v130
	v_add_f32_e32 v130, v156, v130
	v_exp_f32_e32 v210, v133
	v_add_f32_e32 v130, v196, v130
	v_mfma_f32_32x32x16_bf16 v[66:81], v[226:229], v[118:121], v[66:81]
	v_add_f32_e32 v130, v197, v130
	v_exp_f32_e32 v212, v131
	v_add_f32_e32 v130, v198, v130
	v_add_f32_e32 v130, v246, v130
	v_add_f32_e32 v130, v210, v130
	v_add_f32_e32 v130, v211, v130
	v_add_f32_e32 v194, v212, v130
	s_waitcnt lgkmcnt(0)
	v_mfma_f32_32x32x16_bf16 v[82:97], v[146:149], v[126:129], v[82:97]
	v_cvt_pk_bf16_f32 v130, v203, v207
	v_cvt_pk_bf16_f32 v131, v204, v208
	v_cvt_pk_bf16_f32 v132, v205, v209
	v_cvt_pk_bf16_f32 v133, v202, v206
	v_cvt_pk_bf16_f32 v134, v159, v199
	v_cvt_pk_bf16_f32 v135, v160, v200
	v_cvt_pk_bf16_f32 v136, v157, v161
	v_mfma_f32_32x32x16_bf16 v[66:81], v[230:233], v[126:129], v[66:81]
	v_cvt_pk_bf16_f32 v137, v158, v201
	v_cvt_pk_bf16_f32 v138, v144, v145
	v_cvt_pk_bf16_f32 v139, v142, v143
	v_cvt_pk_bf16_f32 v140, v140, v141
	v_cvt_pk_bf16_f32 v141, v154, v155
	v_cvt_pk_bf16_f32 v142, v156, v196
	v_cvt_pk_bf16_f32 v143, v197, v198
	v_mfma_f32_32x32x16_bf16 v[82:97], v[234:237], v[114:117], v[82:97]
	v_cvt_pk_bf16_f32 v144, v246, v210
	v_cvt_pk_bf16_f32 v145, v211, v212
	v_add_u32_e32 v196, s65, v191
	ds_read_b64_tr_b16 v[158:159], v196 offset:0
	ds_read_b64_tr_b16 v[160:161], v196 offset:0x800
	ds_read_b64_tr_b16 v[154:155], v196 offset:0x1000
	ds_read_b64_tr_b16 v[156:157], v196 offset:0x1800
	v_mfma_f32_32x32x16_bf16 v[66:81], v[238:241], v[114:117], v[66:81]
	v_mov_b32_e32 v195, v194
	s_nop 1
	v_permlane32_swap_b32_e32 v194, v195
	v_mfma_f32_32x32x16_bf16 v[82:97], v[150:153], v[122:125], v[82:97]
	ds_read_b64_tr_b16 v[150:151], v196 offset:0x2000
	ds_read_b64_tr_b16 v[152:153], v196 offset:0x2800
	ds_read_b64_tr_b16 v[146:147], v196 offset:0x3000
	ds_read_b64_tr_b16 v[148:149], v196 offset:0x3800
	v_mfma_f32_32x32x16_bf16 v[66:81], v[242:245], v[122:125], v[66:81]
	s_andn2_b64 s[6:7], exec, s[38:39]
	s_andn2_b64 vcc, exec, s[38:39]
	s_cbranch_vccnz .LBB0_411
	s_add_u32 s98, s40, s26
	s_addc_u32 s99, s41, s27
	s_add_u32 s100, s40, s58
	s_addc_u32 s101, s41, s59
	s_add_i32 s4, s36, 0x8000
	s_and_b32 s4, s4, 0x18000
	s_add_i32 s4, s96, s4
	s_waitcnt vmcnt(0) lgkmcnt(0)
	s_barrier
	s_mov_b32 m0, s4
	s_add_i32 s5, s4, 0x4000
	global_load_lds_dwordx4 v170, s[98:99]
	s_mov_b32 m0, s5
	s_nop 0
	global_load_lds_dwordx4 v162, s[100:101]
	s_add_i32 m0, s4, 0x2000
	s_nop 0
	global_load_lds_dwordx4 v172, s[98:99]
	s_add_i32 m0, s4, 0x6000
	s_nop 0
	global_load_lds_dwordx4 v168, s[100:101]
; #define SBAR() __builtin_amdgcn_sched_barrier(0)
; #define ATT_SYNC(jn) do { ATT_WAIT_BAR(); if ((jn) < NT) ATT_DMA((jn), (jn) & 3); } while (0)
; __device__ __forceinline__ void pv_d0_pre(f32x16* o, int vb, s16x4 (&ra)[8], bf16x8 pa0, bf16x8 pa1, bf16x8 pa2, bf16x8 pa3) {
;   s16x4 rb[8];
;   pv_rd<1>(rb, vb);
;   asm volatile("s_waitcnt lgkmcnt(8)" ::: "memory"); SBAR(); pv_mm(o[0], ra, pa0, pa1, pa2, pa3); pv_rd<2>(ra, vb);
;   asm volatile("s_waitcnt lgkmcnt(8)" ::: "memory"); SBAR(); pv_mm(o[1], rb, pa0, pa1, pa2, pa3); pv_rd<3>(rb, vb);
;   asm volatile("s_waitcnt lgkmcnt(8)" ::: "memory"); SBAR(); pv_mm(o[2], ra, pa0, pa1, pa2, pa3);
;   asm volatile("s_waitcnt lgkmcnt(0)" ::: "memory"); SBAR(); pv_mm(o[3], rb, pa0, pa1, pa2, pa3);
; }
; __device__ __forceinline__ void attn_dma_body(const bf16_t* __restrict__ Qb, int ldq, int tpos0, const float* __restrict__ rope, const float* __restrict__ qgain, ...
;     ...
;       finishSM(pA0, pA1, alA, l_reg, pa0, pa1, pa2, pa3); s16x4 va[8]; pv_rd<0>(va, vb0 + ((j - 1) & 3) * (int)SHM_SLOT); SBAR();
;       if (!lead) ATT_SYNC(j + 2);
;       pv_d0_pre(o, vb0 + ((j - 1) & 3) * (int)SHM_SLOT, va, pa0, pa1, pa2, pa3); partialSM(pB0, pB1, m_reg, mnB, alB);
;       if (lead) ATT_SYNC(j + 2);
.LBB0_411:
	ds_read_b64_tr_b16 v[198:199], v196 offset:0x200
	ds_read_b64_tr_b16 v[200:201], v196 offset:0xa00
	ds_read_b64_tr_b16 v[202:203], v196 offset:0x1200
	ds_read_b64_tr_b16 v[204:205], v196 offset:0x1a00
	ds_read_b64_tr_b16 v[206:207], v196 offset:0x2200
	ds_read_b64_tr_b16 v[208:209], v196 offset:0x2a00
	ds_read_b64_tr_b16 v[210:211], v196 offset:0x3200
	ds_read_b64_tr_b16 v[212:213], v196 offset:0x3a00
	s_waitcnt lgkmcnt(8)
	v_mfma_f32_32x32x16_bf16 v[2:17], v[130:133], v[158:161], v[2:17]
	v_mfma_f32_32x32x16_bf16 v[2:17], v[134:137], v[154:157], v[2:17]
	ds_read_b64_tr_b16 v[154:155], v196 offset:0x400
	ds_read_b64_tr_b16 v[156:157], v196 offset:0xc00
	v_mfma_f32_32x32x16_bf16 v[2:17], v[138:141], v[150:153], v[2:17]
	ds_read_b64_tr_b16 v[150:151], v196 offset:0x1400
	ds_read_b64_tr_b16 v[152:153], v196 offset:0x1c00
	ds_read_b64_tr_b16 v[158:159], v196 offset:0x2400
	ds_read_b64_tr_b16 v[160:161], v196 offset:0x2c00
	ds_read_b64_tr_b16 v[214:215], v196 offset:0x3400
	ds_read_b64_tr_b16 v[216:217], v196 offset:0x3c00
	s_waitcnt lgkmcnt(8)
	v_mfma_f32_32x32x16_bf16 v[2:17], v[142:145], v[146:149], v[2:17]
	v_mfma_f32_32x32x16_bf16 v[50:65], v[130:133], v[198:201], v[50:65]
	ds_read_b64_tr_b16 v[146:147], v196 offset:0x600
	ds_read_b64_tr_b16 v[148:149], v196 offset:0xe00
	ds_read_b64_tr_b16 v[198:199], v196 offset:0x1600
	ds_read_b64_tr_b16 v[200:201], v196 offset:0x1e00
	v_mfma_f32_32x32x16_bf16 v[50:65], v[134:137], v[202:205], v[50:65]
	ds_read_b64_tr_b16 v[202:203], v196 offset:0x2600
	ds_read_b64_tr_b16 v[204:205], v196 offset:0x2e00
	v_mfma_f32_32x32x16_bf16 v[50:65], v[138:141], v[206:209], v[50:65]
	ds_read_b64_tr_b16 v[206:207], v196 offset:0x3600
	ds_read_b64_tr_b16 v[208:209], v196 offset:0x3e00
	s_waitcnt lgkmcnt(8)
	v_mfma_f32_32x32x16_bf16 v[50:65], v[142:145], v[210:213], v[50:65]
	v_mfma_f32_32x32x16_bf16 v[34:49], v[130:133], v[154:157], v[34:49]
	s_waitcnt lgkmcnt(0)
	v_mfma_f32_32x32x16_bf16 v[34:49], v[134:137], v[150:153], v[34:49]
	v_mfma_f32_32x32x16_bf16 v[34:49], v[138:141], v[158:161], v[34:49]
	v_mfma_f32_32x32x16_bf16 v[34:49], v[142:145], v[214:217], v[34:49]
	v_mfma_f32_32x32x16_bf16 v[18:33], v[130:133], v[146:149], v[18:33]
	v_max_f32_e32 v150, v83, v83
	v_max_f32_e32 v151, v82, v82
	v_max_f32_e32 v150, v151, v150
	v_max3_f32 v150, v150, v84, v85
	v_max3_f32 v150, v150, v86, v87
	v_max3_f32 v130, v150, v88, v89
	v_max3_f32 v130, v130, v90, v91
	v_mfma_f32_32x32x16_bf16 v[18:33], v[134:137], v[198:201], v[18:33]
	v_max3_f32 v130, v130, v92, v93
	v_max3_f32 v130, v130, v94, v95
	v_max3_f32 v130, v130, v96, v97
	v_max3_f32 v130, v130, v66, v67
	v_max3_f32 v130, v130, v68, v69
	v_max3_f32 v130, v130, v70, v71
	v_max3_f32 v130, v130, v72, v73
	v_mfma_f32_32x32x16_bf16 v[18:33], v[138:141], v[202:205], v[18:33]
	v_max3_f32 v130, v130, v74, v75
	v_max3_f32 v130, v130, v76, v77
	v_max3_f32 v130, v130, v78, v79
	v_max3_f32 v130, v130, v80, v81
	v_mov_b32_e32 v131, v130
	s_nop 1
	v_permlane32_swap_b32_e32 v130, v131
	v_mfma_f32_32x32x16_bf16 v[18:33], v[142:145], v[206:209], v[18:33]
	v_max_f32_e32 v131, v131, v131
	v_max_f32_e32 v130, v130, v130
	v_max_f32_e32 v130, v130, v131
	v_sub_f32_e32 v131, v130, v193
	s_andn2_b64 s[4:5], exec, s[34:35]
	s_andn2_b64 vcc, exec, s[34:35]
	v_cmp_ge_f32_e64 s[8:9], s89, v131
	s_cbranch_vccnz .LBB0_413
	s_add_u32 s98, s40, s26
	s_addc_u32 s99, s41, s27
	s_add_u32 s100, s40, s58
	s_addc_u32 s101, s41, s59
	s_add_i32 s42, s36, 0x8000
	s_and_b32 s42, s42, 0x18000
	s_add_i32 s42, s96, s42
	s_waitcnt vmcnt(0) lgkmcnt(0)
	s_barrier
	s_mov_b32 m0, s42
	s_add_i32 s43, s42, 0x4000
	global_load_lds_dwordx4 v170, s[98:99]
	s_mov_b32 m0, s43
	s_nop 0
	global_load_lds_dwordx4 v162, s[100:101]
	s_add_i32 m0, s42, 0x2000
	s_nop 0
	global_load_lds_dwordx4 v172, s[98:99]
	s_add_i32 m0, s42, 0x6000
	s_nop 0
	global_load_lds_dwordx4 v168, s[100:101]

; #define SBAR() __builtin_amdgcn_sched_barrier(0)
; #define ATT_SYNC(jn) do { ATT_WAIT_BAR(); if ((jn) < NT) ATT_DMA((jn), (jn) & 3); } while (0)
; __device__ __forceinline__ void partialSM(f32x16& p0, f32x16& p1, float& m_reg, float& mn, float& alpha) {
;     ...
;   else { mn = fmaxf(m_reg, pmax); alpha = __builtin_amdgcn_exp2f((m_reg - mn) * C); m_reg = mn; }
;   float mnC = -mn * C;
;   for (int r = 0; r < 16; ++r) p0[r] = fmaf(p0[r], C, mnC); for (int r = 0; r < 16; ++r) p1[r] = fmaf(p1[r], C, mnC);
;   for (int r = 0; r < 16; ++r) p0[r] = __builtin_amdgcn_exp2f(p0[r]);
; }
; __device__ __forceinline__ void finishSM(f32x16& p0, f32x16& p1, float alpha, float& l_reg, bf16x8& pa0, bf16x8& pa1, bf16x8& pa2, bf16x8& pa3) {
;   for (int r = 0; r < 16; ++r) p1[r] = __builtin_amdgcn_exp2f(p1[r]);
;   float ps = 0; for (int r = 0; r < 16; ++r) ps += p0[r]; for (int r = 0; r < 16; ++r) ps += p1[r];
;   { auto rr = __builtin_amdgcn_permlane32_swap(__float_as_uint(ps), __float_as_uint(ps), false, false);
;     ps = __uint_as_float(rr[0]) + __uint_as_float(rr[1]); }
;   l_reg = l_reg * alpha + ps;
;     ...
;   PK4(p0, 0, pa0); PK4(p0, 8, pa1); PK4(p1, 0, pa2); PK4(p1, 8, pa3);
;     ...
; }
; __device__ __forceinline__ void attn_dma_body(const bf16_t* __restrict__ Qb, int ldq, int tpos0, const float* __restrict__ rope, const float* __restrict__ qgain, ...
;     ...
;     { SBAR(); qkt(pA0, pA1, (const bf16_t*)(lds + ((j + 1) & 3) * SHM_SLOT), qr, r32, hi);
;       finishSM(pB0, pB1, alB, l_reg, pa0, pa1, pa2, pa3); s16x4 va[8]; pv_rd<0>(va, vb0 + (j & 3) * (int)SHM_SLOT); SBAR();
;       if (!lead) ATT_SYNC(j + 3);
.LBB0_417:
	v_cndmask_b32_e64 v193, v130, v193, s[8:9]
	v_mul_f32_e32 v197, 0xbe0293ee, v193
	v_fmamk_f32 v82, v82, 0x3e0293ee, v197
	v_fmamk_f32 v83, v83, 0x3e0293ee, v197
	v_fmamk_f32 v84, v84, 0x3e0293ee, v197
	v_fmamk_f32 v85, v85, 0x3e0293ee, v197
	v_fmamk_f32 v86, v86, 0x3e0293ee, v197
	v_fmamk_f32 v87, v87, 0x3e0293ee, v197
	v_fmamk_f32 v88, v88, 0x3e0293ee, v197
	v_fmamk_f32 v89, v89, 0x3e0293ee, v197
	v_fmamk_f32 v90, v90, 0x3e0293ee, v197
	v_fmamk_f32 v91, v91, 0x3e0293ee, v197
	v_fmamk_f32 v92, v92, 0x3e0293ee, v197
	v_fmamk_f32 v93, v93, 0x3e0293ee, v197
	v_fmamk_f32 v94, v94, 0x3e0293ee, v197
	v_fmamk_f32 v95, v95, 0x3e0293ee, v197
	v_fmamk_f32 v96, v96, 0x3e0293ee, v197
	v_fmamk_f32 v97, v97, 0x3e0293ee, v197
	v_fmamk_f32 v198, v66, 0x3e0293ee, v197
	v_fmamk_f32 v199, v67, 0x3e0293ee, v197
	v_fmamk_f32 v220, v68, 0x3e0293ee, v197
	v_fmamk_f32 v221, v69, 0x3e0293ee, v197
	v_fmamk_f32 v222, v70, 0x3e0293ee, v197
	v_fmamk_f32 v223, v71, 0x3e0293ee, v197
	v_fmamk_f32 v224, v72, 0x3e0293ee, v197
	v_fmamk_f32 v225, v73, 0x3e0293ee, v197
	v_fmamk_f32 v226, v74, 0x3e0293ee, v197
	v_fmamk_f32 v227, v75, 0x3e0293ee, v197
	v_fmamk_f32 v228, v76, 0x3e0293ee, v197
	v_fmamk_f32 v229, v77, 0x3e0293ee, v197
	v_fmamk_f32 v230, v78, 0x3e0293ee, v197
	v_fmamk_f32 v231, v79, 0x3e0293ee, v197
	v_fmamk_f32 v248, v80, 0x3e0293ee, v197
	v_fmac_f32_e32 v197, 0x3e0293ee, v81
	s_add_i32 s97, s97, 2
	v_exp_f32_e32 v232, v82
	v_exp_f32_e32 v233, v83
	v_exp_f32_e32 v234, v84
	v_exp_f32_e32 v235, v85
	v_exp_f32_e32 v236, v86
	v_exp_f32_e32 v237, v87
	v_exp_f32_e32 v238, v88
	v_exp_f32_e32 v239, v89
	v_exp_f32_e32 v240, v90
	v_exp_f32_e32 v241, v91
	v_exp_f32_e32 v242, v92
	v_exp_f32_e32 v243, v93
	v_exp_f32_e32 v244, v94
	v_exp_f32_e32 v245, v95
	v_exp_f32_e32 v246, v96
	v_exp_f32_e32 v247, v97
	s_and_b32 s8, s36, 0x18000
	s_add_i32 s8, s8, 0
	v_add_u32_e32 v70, s8, v183
	ds_read_b128 v[66:69], v70
	ds_read_b128 v[70:73], v70 offset:8192
	v_add_u32_e32 v142, s8, v186
	v_add_u32_e32 v150, s8, v185
	v_add_u32_e32 v158, s8, v187
	s_waitcnt lgkmcnt(0)
	v_mfma_f32_32x32x16_bf16 v[82:97], v[66:69], v[102:105], 0
	v_add_u32_e32 v66, s8, v184
	ds_read_b128 v[130:133], v66
	ds_read_b128 v[134:137], v66 offset:8192
	ds_read_b128 v[138:141], v142
	ds_read_b128 v[142:145], v142 offset:8192
	ds_read_b128 v[146:149], v150
	ds_read_b128 v[150:153], v150 offset:8192
	ds_read_b128 v[154:157], v158
	ds_read_b128 v[158:161], v158 offset:8192
	v_add_u32_e32 v200, s8, v188
	v_exp_f32_e32 v249, v198
	v_exp_f32_e32 v199, v199
	v_exp_f32_e32 v220, v220
	v_mfma_f32_32x32x16_bf16 v[66:81], v[70:73], v[102:105], 0
	v_exp_f32_e32 v221, v221
	v_exp_f32_e32 v222, v222
	v_exp_f32_e32 v223, v223
	v_add_u32_e32 v208, s8, v189
	v_add_u32_e32 v216, s8, v190
	s_waitcnt lgkmcnt(0)
	v_mfma_f32_32x32x16_bf16 v[82:97], v[130:133], v[110:113], v[82:97]
	ds_read_b128 v[130:133], v200
	ds_read_b128 v[200:203], v200 offset:8192
	ds_read_b128 v[204:207], v208
	ds_read_b128 v[208:211], v208 offset:8192
	ds_read_b128 v[212:215], v216
	ds_read_b128 v[216:219], v216 offset:8192
	v_mfma_f32_32x32x16_bf16 v[66:81], v[134:137], v[110:113], v[66:81]
	v_add_f32_e32 v134, v233, v232
	v_add_f32_e32 v134, v234, v134
	v_add_f32_e32 v134, v235, v134
	v_add_f32_e32 v134, v236, v134
	v_add_f32_e32 v134, v237, v134
	v_add_f32_e32 v134, v238, v134
	v_mfma_f32_32x32x16_bf16 v[82:97], v[138:141], v[98:101], v[82:97]
	v_add_f32_e32 v134, v239, v134
	v_add_f32_e32 v134, v240, v134
	v_add_f32_e32 v134, v241, v134
	v_add_f32_e32 v134, v242, v134
	v_add_f32_e32 v134, v243, v134
	v_add_f32_e32 v134, v244, v134
	v_add_f32_e32 v134, v245, v134
	v_mfma_f32_32x32x16_bf16 v[66:81], v[142:145], v[98:101], v[66:81]
	v_add_f32_e32 v134, v246, v134
	v_add_f32_e32 v134, v247, v134
	v_add_f32_e32 v134, v249, v134
	v_add_f32_e32 v134, v199, v134
	v_exp_f32_e32 v138, v224
	v_add_f32_e32 v134, v220, v134
	v_exp_f32_e32 v139, v225
	v_mfma_f32_32x32x16_bf16 v[82:97], v[146:149], v[106:109], v[82:97]
	v_add_f32_e32 v134, v221, v134
	v_exp_f32_e32 v140, v226
	v_add_f32_e32 v134, v222, v134
	v_exp_f32_e32 v141, v227
	v_add_f32_e32 v134, v223, v134
	v_exp_f32_e32 v224, v228
	v_add_f32_e32 v134, v138, v134
	v_mfma_f32_32x32x16_bf16 v[66:81], v[150:153], v[106:109], v[66:81]
	v_exp_f32_e32 v225, v229
	v_add_f32_e32 v134, v139, v134
	v_exp_f32_e32 v226, v230
	v_add_f32_e32 v134, v140, v134
	v_exp_f32_e32 v227, v231
	v_add_f32_e32 v134, v141, v134
	v_exp_f32_e32 v228, v248
	v_mfma_f32_32x32x16_bf16 v[82:97], v[154:157], v[118:121], v[82:97]
	v_add_f32_e32 v134, v224, v134
	v_exp_f32_e32 v229, v197
	v_add_f32_e32 v134, v225, v134
	v_add_f32_e32 v134, v226, v134
	v_add_f32_e32 v134, v227, v134
	v_add_f32_e32 v134, v228, v134
	v_add_f32_e32 v197, v229, v134
	v_mfma_f32_32x32x16_bf16 v[66:81], v[158:161], v[118:121], v[66:81]
	v_mov_b32_e32 v198, v197
	s_nop 1
	v_permlane32_swap_b32_e32 v197, v198
	s_waitcnt lgkmcnt(0)
	v_mfma_f32_32x32x16_bf16 v[82:97], v[130:133], v[126:129], v[82:97]
	v_cvt_pk_bf16_f32 v130, v232, v233
	v_cvt_pk_bf16_f32 v131, v234, v235
	v_cvt_pk_bf16_f32 v132, v236, v237
	v_cvt_pk_bf16_f32 v133, v238, v239
	v_cvt_pk_bf16_f32 v134, v240, v241
	v_cvt_pk_bf16_f32 v135, v242, v243
	v_cvt_pk_bf16_f32 v136, v244, v245
	v_mfma_f32_32x32x16_bf16 v[66:81], v[200:203], v[126:129], v[66:81]
	v_cvt_pk_bf16_f32 v137, v246, v247
	v_cvt_pk_bf16_f32 v142, v249, v199
	v_cvt_pk_bf16_f32 v143, v220, v221
	v_cvt_pk_bf16_f32 v144, v222, v223
	v_cvt_pk_bf16_f32 v145, v138, v139
	v_cvt_pk_bf16_f32 v138, v140, v141
	v_cvt_pk_bf16_f32 v139, v224, v225
	v_mfma_f32_32x32x16_bf16 v[82:97], v[204:207], v[114:117], v[82:97]
	v_cvt_pk_bf16_f32 v140, v226, v227
	v_cvt_pk_bf16_f32 v141, v228, v229
	v_add_u32_e32 v199, s69, v191
	ds_read_b64_tr_b16 v[158:159], v199 offset:0
	ds_read_b64_tr_b16 v[160:161], v199 offset:0x800
	ds_read_b64_tr_b16 v[154:155], v199 offset:0x1000
	ds_read_b64_tr_b16 v[156:157], v199 offset:0x1800
	v_mfma_f32_32x32x16_bf16 v[66:81], v[208:211], v[114:117], v[66:81]
	ds_read_b64_tr_b16 v[150:151], v199 offset:0x2000
	ds_read_b64_tr_b16 v[152:153], v199 offset:0x2800
	ds_read_b64_tr_b16 v[146:147], v199 offset:0x3000
	ds_read_b64_tr_b16 v[148:149], v199 offset:0x3800
	v_mfma_f32_32x32x16_bf16 v[82:97], v[212:215], v[122:125], v[82:97]
	v_mfma_f32_32x32x16_bf16 v[66:81], v[216:219], v[122:125], v[66:81]
	s_and_b64 vcc, exec, s[6:7]
	s_cbranch_vccnz .LBB0_420
	s_waitcnt vmcnt(0) lgkmcnt(0)
	s_barrier
	s_cmpk_gt_u32 s97, 0x80
	s_cbranch_scc1 .LBB0_420
	s_add_u32 s98, s40, s60
	s_addc_u32 s99, s41, s61
	s_add_u32 s100, s40, s62
	s_addc_u32 s101, s41, s63
	s_add_i32 s6, s96, s65
	s_mov_b32 m0, s6
	s_add_i32 s7, s6, 0x4000
	global_load_lds_dwordx4 v170, s[98:99]
	s_mov_b32 m0, s7
	s_nop 0
	global_load_lds_dwordx4 v162, s[100:101]
	s_add_i32 m0, s6, 0x2000
	s_nop 0
	global_load_lds_dwordx4 v172, s[98:99]
	s_add_i32 m0, s6, 0x6000
	s_nop 0
	global_load_lds_dwordx4 v168, s[100:101]
; #define SBAR() __builtin_amdgcn_sched_barrier(0)
; #define RESC(a) do { if (__any((a) < 1.f)) { if (hi == 0) al_l[r32] = (a); asm volatile("s_waitcnt lgkmcnt(0)" ::: "memory"); \
;     for (int d = 0; d < 4; ++d) for (int r = 0; r < 16; ++r) o[d][r] *= al_l[crow(r, hi)]; } } while (0)
; #define RESC(a) do { if (__any((a) < 1.f)) { if (hi == 0) al_l[r32] = (a); asm volatile("s_waitcnt lgkmcnt(0)" ::: "memory"); \
;     for (int d = 0; d < 4; ++d) for (int r = 0; r < 16; ++r) o[d][r] *= al_l[crow(r, hi)]; } } while (0)
; #define ATT_SYNC(jn) do { ATT_WAIT_BAR(); if ((jn) < NT) ATT_DMA((jn), (jn) & 3); } while (0)
; __device__ __forceinline__ void pv_d0_pre(f32x16* o, int vb, s16x4 (&ra)[8], bf16x8 pa0, bf16x8 pa1, bf16x8 pa2, bf16x8 pa3) {
;   s16x4 rb[8];
;   pv_rd<1>(rb, vb);
;   asm volatile("s_waitcnt lgkmcnt(8)" ::: "memory"); SBAR(); pv_mm(o[0], ra, pa0, pa1, pa2, pa3); pv_rd<2>(ra, vb);
;   asm volatile("s_waitcnt lgkmcnt(8)" ::: "memory"); SBAR(); pv_mm(o[1], rb, pa0, pa1, pa2, pa3); pv_rd<3>(rb, vb);
;   asm volatile("s_waitcnt lgkmcnt(8)" ::: "memory"); SBAR(); pv_mm(o[2], ra, pa0, pa1, pa2, pa3);
;   asm volatile("s_waitcnt lgkmcnt(0)" ::: "memory"); SBAR(); pv_mm(o[3], rb, pa0, pa1, pa2, pa3);
; }
; __device__ __forceinline__ void attn_dma_body(const bf16_t* __restrict__ Qb, int ldq, int tpos0, const float* __restrict__ rope, const float* __restrict__ qgain, ...
;     ...
;       if (!lead) ATT_SYNC(j + 3);
;       pv_d0_pre(o, vb0 + (j & 3) * (int)SHM_SLOT, va, pa0, pa1, pa2, pa3); partialSM(pA0, pA1, m_reg, mnA, alA);
;       if (lead) ATT_SYNC(j + 3);
;       RESC(alA); }
.LBB0_420:
	ds_read_b64_tr_b16 v[200:201], v199 offset:0x200
	ds_read_b64_tr_b16 v[202:203], v199 offset:0xa00
	ds_read_b64_tr_b16 v[204:205], v199 offset:0x1200
	ds_read_b64_tr_b16 v[206:207], v199 offset:0x1a00
	ds_read_b64_tr_b16 v[208:209], v199 offset:0x2200
	ds_read_b64_tr_b16 v[210:211], v199 offset:0x2a00
	ds_read_b64_tr_b16 v[212:213], v199 offset:0x3200
	ds_read_b64_tr_b16 v[214:215], v199 offset:0x3a00
	s_waitcnt lgkmcnt(8)
	v_mfma_f32_32x32x16_bf16 v[2:17], v[130:133], v[158:161], v[2:17]
	v_mfma_f32_32x32x16_bf16 v[2:17], v[134:137], v[154:157], v[2:17]
	ds_read_b64_tr_b16 v[154:155], v199 offset:0x400
	ds_read_b64_tr_b16 v[156:157], v199 offset:0xc00
	v_mfma_f32_32x32x16_bf16 v[2:17], v[142:145], v[150:153], v[2:17]
	ds_read_b64_tr_b16 v[150:151], v199 offset:0x1400
	ds_read_b64_tr_b16 v[152:153], v199 offset:0x1c00
	ds_read_b64_tr_b16 v[158:159], v199 offset:0x2400
	ds_read_b64_tr_b16 v[160:161], v199 offset:0x2c00
	ds_read_b64_tr_b16 v[216:217], v199 offset:0x3400
	ds_read_b64_tr_b16 v[218:219], v199 offset:0x3c00
	s_waitcnt lgkmcnt(8)
	v_mfma_f32_32x32x16_bf16 v[2:17], v[138:141], v[146:149], v[2:17]
	v_mfma_f32_32x32x16_bf16 v[50:65], v[130:133], v[200:203], v[50:65]
	ds_read_b64_tr_b16 v[146:147], v199 offset:0x600
	ds_read_b64_tr_b16 v[148:149], v199 offset:0xe00
	ds_read_b64_tr_b16 v[200:201], v199 offset:0x1600
	ds_read_b64_tr_b16 v[202:203], v199 offset:0x1e00
	v_mfma_f32_32x32x16_bf16 v[50:65], v[134:137], v[204:207], v[50:65]
	ds_read_b64_tr_b16 v[204:205], v199 offset:0x2600
	ds_read_b64_tr_b16 v[206:207], v199 offset:0x2e00
	v_mfma_f32_32x32x16_bf16 v[50:65], v[142:145], v[208:211], v[50:65]
	ds_read_b64_tr_b16 v[208:209], v199 offset:0x3600
	ds_read_b64_tr_b16 v[210:211], v199 offset:0x3e00
	s_waitcnt lgkmcnt(8)
	v_mfma_f32_32x32x16_bf16 v[50:65], v[138:141], v[212:215], v[50:65]
	v_mfma_f32_32x32x16_bf16 v[34:49], v[130:133], v[154:157], v[34:49]
	s_waitcnt lgkmcnt(0)
	v_mfma_f32_32x32x16_bf16 v[34:49], v[134:137], v[150:153], v[34:49]
	v_mfma_f32_32x32x16_bf16 v[34:49], v[142:145], v[158:161], v[34:49]
	v_mfma_f32_32x32x16_bf16 v[34:49], v[138:141], v[216:219], v[34:49]
	v_mfma_f32_32x32x16_bf16 v[18:33], v[130:133], v[146:149], v[18:33]
	v_max_f32_e32 v150, v83, v83
	v_max_f32_e32 v151, v82, v82
	v_max_f32_e32 v150, v151, v150
	v_max3_f32 v150, v150, v84, v85
	v_max3_f32 v150, v150, v86, v87
	v_max3_f32 v130, v150, v88, v89
	v_max3_f32 v130, v130, v90, v91
	v_mfma_f32_32x32x16_bf16 v[18:33], v[134:137], v[200:203], v[18:33]
	v_max3_f32 v130, v130, v92, v93
	v_max3_f32 v130, v130, v94, v95
	v_max3_f32 v130, v130, v96, v97
	v_max3_f32 v130, v130, v66, v67
	v_max3_f32 v130, v130, v68, v69
	v_max3_f32 v130, v130, v70, v71
	v_max3_f32 v130, v130, v72, v73
	v_mfma_f32_32x32x16_bf16 v[18:33], v[142:145], v[204:207], v[18:33]
	v_max3_f32 v130, v130, v74, v75
	v_max3_f32 v130, v130, v76, v77
	v_max3_f32 v130, v130, v78, v79
	v_max3_f32 v130, v130, v80, v81
	v_mov_b32_e32 v131, v130
	s_nop 1
	v_permlane32_swap_b32_e32 v130, v131
	v_mfma_f32_32x32x16_bf16 v[18:33], v[138:141], v[208:211], v[18:33]
	v_max_f32_e32 v131, v131, v131
	v_max_f32_e32 v130, v130, v130
	v_max_f32_e32 v130, v130, v131
	v_sub_f32_e32 v131, v130, v193
	v_cmp_ge_f32_e32 vcc, s89, v131
	s_cmp_eq_u64 vcc, exec
	s_cselect_b64 s[6:7], -1, 0
	s_and_b64 vcc, exec, s[4:5]
	s_cbranch_vccnz .LBB0_423
	s_waitcnt vmcnt(0) lgkmcnt(0)
	s_barrier
	s_cmpk_gt_u32 s97, 0x80
	s_cbranch_scc1 .LBB0_423
	s_add_u32 s98, s40, s60
	s_addc_u32 s99, s41, s61
	s_add_u32 s100, s40, s62
	s_addc_u32 s101, s41, s63
	s_add_i32 s4, s96, s65
	s_mov_b32 m0, s4
	s_add_i32 s5, s4, 0x4000
	global_load_lds_dwordx4 v170, s[98:99]
	s_mov_b32 m0, s5
	s_nop 0
	global_load_lds_dwordx4 v162, s[100:101]
	s_add_i32 m0, s4, 0x2000
	s_nop 0
	global_load_lds_dwordx4 v172, s[98:99]
	s_add_i32 m0, s4, 0x6000
	s_nop 0
	global_load_lds_dwordx4 v168, s[100:101]

; #define SBAR() __builtin_amdgcn_sched_barrier(0)
; __device__ __forceinline__ void finishSM(f32x16& p0, f32x16& p1, float alpha, float& l_reg, bf16x8& pa0, bf16x8& pa1, bf16x8& pa2, bf16x8& pa3) {
;   for (int r = 0; r < 16; ++r) p1[r] = __builtin_amdgcn_exp2f(p1[r]);
;   float ps = 0; for (int r = 0; r < 16; ++r) ps += p0[r]; for (int r = 0; r < 16; ++r) ps += p1[r];
;   { auto rr = __builtin_amdgcn_permlane32_swap(__float_as_uint(ps), __float_as_uint(ps), false, false);
;     ps = __uint_as_float(rr[0]) + __uint_as_float(rr[1]); }
;   l_reg = l_reg * alpha + ps;
;     ...
;   PK4(p0, 0, pa0); PK4(p0, 8, pa1); PK4(p1, 0, pa2); PK4(p1, 8, pa3);
;     ...
; }
; __device__ __forceinline__ void attn_dma_body(const bf16_t* __restrict__ Qb, int ldq, int tpos0, const float* __restrict__ rope, const float* __restrict__ qgain, ...
;     ...
;   { SBAR(); qkt(pB0, pB1, (const bf16_t*)(lds + ((NT - 1) & 3) * SHM_SLOT), qr, r32, hi);
;     finishSM(pA0, pA1, alA, l_reg, pa0, pa1, pa2, pa3); SBAR();
.LBB0_429:
	s_add_i32 s4, 0, 0x18000
	v_add_u32_e32 v70, s4, v183
	ds_read_b128 v[66:69], v70
	ds_read_b128 v[70:73], v70 offset:8192
	v_add_u32_e32 v147, s4, v186
	v_add_u32_e32 v156, s4, v187
	v_exp_f32_e32 v144, v144
	s_waitcnt lgkmcnt(0)
	v_mfma_f32_32x32x16_bf16 v[82:97], v[66:69], v[102:105], 0
	v_add_u32_e32 v66, s4, v184
	ds_read_b128 v[148:151], v66
	ds_read_b128 v[152:155], v66 offset:8192
	v_exp_f32_e32 v145, v145
	v_exp_f32_e32 v142, v142
	v_exp_f32_e32 v143, v143
	v_exp_f32_e32 v140, v140
	v_exp_f32_e32 v141, v141
	v_mfma_f32_32x32x16_bf16 v[66:81], v[70:73], v[102:105], 0
	ds_read_b128 v[102:105], v147
	ds_read_b128 v[168:171], v147 offset:8192
	v_add_u32_e32 v147, s4, v185
	ds_read_b128 v[184:187], v147
	ds_read_b128 v[194:197], v147 offset:8192
	ds_read_b128 v[210:213], v156
	ds_read_b128 v[214:217], v156 offset:8192
	v_add_u32_e32 v147, s4, v188
	v_exp_f32_e32 v138, v138
	v_exp_f32_e32 v139, v139
	v_exp_f32_e32 v136, v136
	s_waitcnt lgkmcnt(0)
	v_mfma_f32_32x32x16_bf16 v[82:97], v[148:151], v[110:113], v[82:97]
	ds_read_b128 v[148:151], v147
	ds_read_b128 v[218:221], v147 offset:8192
	v_add_u32_e32 v147, s4, v189
	ds_read_b128 v[222:225], v147
	ds_read_b128 v[226:229], v147 offset:8192
	v_add_u32_e32 v147, s4, v190
	v_exp_f32_e32 v137, v137
	v_exp_f32_e32 v134, v134
	v_exp_f32_e32 v135, v135
	v_mfma_f32_32x32x16_bf16 v[66:81], v[152:155], v[110:113], v[66:81]
	ds_read_b128 v[110:113], v147
	ds_read_b128 v[152:155], v147 offset:8192
	v_exp_f32_e32 v132, v132
	v_exp_f32_e32 v133, v133
	v_exp_f32_e32 v130, v130
	v_exp_f32_e32 v131, v131
	v_mfma_f32_32x32x16_bf16 v[82:97], v[102:105], v[98:101], v[82:97]
	v_mfma_f32_32x32x16_bf16 v[66:81], v[168:171], v[98:101], v[66:81]
	v_add_f32_e32 v98, 0, v203
	v_add_f32_e32 v98, v207, v98
	v_add_f32_e32 v98, v204, v98
	v_add_f32_e32 v98, v208, v98
	v_add_f32_e32 v98, v205, v98
	v_add_f32_e32 v98, v209, v98
	v_add_f32_e32 v98, v202, v98
	v_mfma_f32_32x32x16_bf16 v[82:97], v[184:187], v[106:109], v[82:97]
	v_add_f32_e32 v98, v206, v98
	v_add_f32_e32 v98, v159, v98
	v_add_f32_e32 v98, v199, v98
	v_add_f32_e32 v98, v160, v98
	v_add_f32_e32 v98, v200, v98
	v_add_f32_e32 v98, v157, v98
	v_add_f32_e32 v98, v161, v98
	v_mfma_f32_32x32x16_bf16 v[66:81], v[194:197], v[106:109], v[66:81]
	v_add_f32_e32 v98, v158, v98
	v_add_f32_e32 v98, v201, v98
	v_add_f32_e32 v98, v144, v98
	v_add_f32_e32 v98, v145, v98
	v_add_f32_e32 v98, v142, v98
	v_add_f32_e32 v98, v143, v98
	v_add_f32_e32 v98, v140, v98
	v_mfma_f32_32x32x16_bf16 v[82:97], v[210:213], v[118:121], v[82:97]
	v_add_f32_e32 v98, v141, v98
	v_add_f32_e32 v98, v138, v98
	v_add_f32_e32 v98, v139, v98
	v_add_f32_e32 v98, v136, v98
	v_add_f32_e32 v98, v137, v98
	v_add_f32_e32 v98, v134, v98
	v_add_f32_e32 v98, v135, v98
	v_mfma_f32_32x32x16_bf16 v[66:81], v[214:217], v[118:121], v[66:81]
	v_add_f32_e32 v98, v132, v98
	v_add_f32_e32 v98, v133, v98
	v_add_f32_e32 v98, v130, v98
	v_add_f32_e32 v98, v131, v98
	v_mov_b32_e32 v99, v98
	v_cvt_pk_bf16_f32 v100, v203, v207
	v_cvt_pk_bf16_f32 v101, v204, v208
	s_waitcnt lgkmcnt(0)
	v_mfma_f32_32x32x16_bf16 v[82:97], v[148:151], v[126:129], v[82:97]
	v_cvt_pk_bf16_f32 v102, v205, v209
	v_cvt_pk_bf16_f32 v103, v202, v206
	v_permlane32_swap_b32_e32 v98, v99
	v_mfma_f32_32x32x16_bf16 v[66:81], v[218:221], v[126:129], v[66:81]
	v_cvt_pk_bf16_f32 v104, v159, v199
	v_cvt_pk_bf16_f32 v105, v160, v200
	v_cvt_pk_bf16_f32 v106, v157, v161
	v_cvt_pk_bf16_f32 v107, v158, v201
	v_cvt_pk_bf16_f32 v118, v144, v145
	v_cvt_pk_bf16_f32 v119, v142, v143
	v_cvt_pk_bf16_f32 v120, v140, v141
	v_mfma_f32_32x32x16_bf16 v[82:97], v[222:225], v[114:117], v[82:97]
	v_cvt_pk_bf16_f32 v121, v138, v139
	v_cvt_pk_bf16_f32 v108, v136, v137
	v_cvt_pk_bf16_f32 v109, v134, v135
	v_mfma_f32_32x32x16_bf16 v[66:81], v[226:229], v[114:117], v[66:81]
	v_mfma_f32_32x32x16_bf16 v[82:97], v[110:113], v[122:125], v[82:97]
	v_cvt_pk_bf16_f32 v110, v132, v133
	v_cvt_pk_bf16_f32 v111, v130, v131
	s_nop 0
	v_mfma_f32_32x32x16_bf16 v[66:81], v[152:155], v[122:125], v[66:81]
	s_cmp_lg_u32 0, -1
	s_cselect_b32 s4, 0, 0
	s_add_i32 s4, s4, 0x14000
	v_add_u32_e32 v116, s4, v181
	ds_read_b64_tr_b16 v[112:113], v116 offset:0
	ds_read_b64_tr_b16 v[114:115], v116 offset:0x800
	ds_read_b64_tr_b16 v[122:123], v116 offset:0x1000
	ds_read_b64_tr_b16 v[124:125], v116 offset:0x1800
	ds_read_b64_tr_b16 v[126:127], v116 offset:0x2000
	ds_read_b64_tr_b16 v[128:129], v116 offset:0x2800
	ds_read_b64_tr_b16 v[130:131], v116 offset:0x3000
	ds_read_b64_tr_b16 v[132:133], v116 offset:0x3800
	ds_read_b64_tr_b16 v[134:135], v116 offset:0x200
	ds_read_b64_tr_b16 v[136:137], v116 offset:0xa00
	ds_read_b64_tr_b16 v[138:139], v116 offset:0x1200
	ds_read_b64_tr_b16 v[140:141], v116 offset:0x1a00
	ds_read_b64_tr_b16 v[142:143], v116 offset:0x2200
	ds_read_b64_tr_b16 v[144:145], v116 offset:0x2a00
	ds_read_b64_tr_b16 v[148:149], v116 offset:0x3200
	ds_read_b64_tr_b16 v[150:151], v116 offset:0x3a00
	s_waitcnt lgkmcnt(8)
; #define SBAR() __builtin_amdgcn_sched_barrier(0)
; #define RESC(a) do { if (__any((a) < 1.f)) { if (hi == 0) al_l[r32] = (a); asm volatile("s_waitcnt lgkmcnt(0)" ::: "memory"); \
;     for (int d = 0; d < 4; ++d) for (int r = 0; r < 16; ++r) o[d][r] *= al_l[crow(r, hi)]; } } while (0)
; #define RESC(a) do { if (__any((a) < 1.f)) { if (hi == 0) al_l[r32] = (a); asm volatile("s_waitcnt lgkmcnt(0)" ::: "memory"); \
;     for (int d = 0; d < 4; ++d) for (int r = 0; r < 16; ++r) o[d][r] *= al_l[crow(r, hi)]; } } while (0)
; __device__ __forceinline__ void pv_d0(f32x16* o, int vb, bf16x8 pa0, bf16x8 pa1, bf16x8 pa2, bf16x8 pa3) {
;   s16x4 ra[8], rb[8];
;   pv_rd<0>(ra, vb); pv_rd<1>(rb, vb);
;   asm volatile("s_waitcnt lgkmcnt(8)" ::: "memory"); SBAR(); pv_mm(o[0], ra, pa0, pa1, pa2, pa3); pv_rd<2>(ra, vb);
;   asm volatile("s_waitcnt lgkmcnt(8)" ::: "memory"); SBAR(); pv_mm(o[1], rb, pa0, pa1, pa2, pa3); pv_rd<3>(rb, vb);
;   asm volatile("s_waitcnt lgkmcnt(8)" ::: "memory"); SBAR(); pv_mm(o[2], ra, pa0, pa1, pa2, pa3);
;   asm volatile("s_waitcnt lgkmcnt(0)" ::: "memory"); SBAR(); pv_mm(o[3], rb, pa0, pa1, pa2, pa3);
; }
; __device__ __forceinline__ void attn_dma_body(const bf16_t* __restrict__ Qb, int ldq, int tpos0, const float* __restrict__ rope, const float* __restrict__ qgain, ...
;     ...
;     pv_d0(o, vb0 + ((NT - 2) & 3) * (int)SHM_SLOT, pa0, pa1, pa2, pa3); partialSM(pB0, pB1, m_reg, mnB, alB);
;     RESC(alB);
	s_nop 0
	v_mfma_f32_32x32x16_bf16 v[2:17], v[100:103], v[112:115], v[2:17]
	ds_read_b64_tr_b16 v[112:113], v116 offset:0x400
	ds_read_b64_tr_b16 v[114:115], v116 offset:0xc00
	v_mfma_f32_32x32x16_bf16 v[2:17], v[104:107], v[122:125], v[2:17]
	ds_read_b64_tr_b16 v[122:123], v116 offset:0x1400
	ds_read_b64_tr_b16 v[124:125], v116 offset:0x1c00
	v_mfma_f32_32x32x16_bf16 v[2:17], v[118:121], v[126:129], v[2:17]
	ds_read_b64_tr_b16 v[126:127], v116 offset:0x2400
	ds_read_b64_tr_b16 v[128:129], v116 offset:0x2c00
	ds_read_b64_tr_b16 v[152:153], v116 offset:0x3400
	ds_read_b64_tr_b16 v[154:155], v116 offset:0x3c00
	s_waitcnt lgkmcnt(8)
	v_mfma_f32_32x32x16_bf16 v[2:17], v[108:111], v[130:133], v[2:17]
	v_mfma_f32_32x32x16_bf16 v[50:65], v[100:103], v[134:137], v[50:65]
	ds_read_b64_tr_b16 v[130:131], v116 offset:0x600
	ds_read_b64_tr_b16 v[132:133], v116 offset:0xe00
	ds_read_b64_tr_b16 v[134:135], v116 offset:0x1600
	ds_read_b64_tr_b16 v[136:137], v116 offset:0x1e00
	v_mfma_f32_32x32x16_bf16 v[50:65], v[104:107], v[138:141], v[50:65]
	ds_read_b64_tr_b16 v[138:139], v116 offset:0x2600
	ds_read_b64_tr_b16 v[140:141], v116 offset:0x2e00
	v_mfma_f32_32x32x16_bf16 v[50:65], v[118:121], v[142:145], v[50:65]
	ds_read_b64_tr_b16 v[142:143], v116 offset:0x3600
	ds_read_b64_tr_b16 v[144:145], v116 offset:0x3e00
	s_waitcnt lgkmcnt(8)
	v_mfma_f32_32x32x16_bf16 v[50:65], v[108:111], v[148:151], v[50:65]
	v_mfma_f32_32x32x16_bf16 v[34:49], v[100:103], v[112:115], v[34:49]
	s_waitcnt lgkmcnt(0)
	v_mfma_f32_32x32x16_bf16 v[34:49], v[104:107], v[122:125], v[34:49]
	v_mfma_f32_32x32x16_bf16 v[34:49], v[118:121], v[126:129], v[34:49]
	v_mfma_f32_32x32x16_bf16 v[34:49], v[108:111], v[152:155], v[34:49]
	v_mfma_f32_32x32x16_bf16 v[18:33], v[100:103], v[130:133], v[18:33]
	v_max_f32_e32 v112, v83, v83
	v_max_f32_e32 v113, v82, v82
	v_max_f32_e32 v112, v113, v112
	v_max3_f32 v112, v112, v84, v85
	v_max3_f32 v112, v112, v86, v87
	v_max3_f32 v100, v112, v88, v89
	v_max3_f32 v100, v100, v90, v91
	v_max3_f32 v100, v100, v92, v93
	v_mfma_f32_32x32x16_bf16 v[18:33], v[104:107], v[134:137], v[18:33]
	v_max3_f32 v100, v100, v94, v95
	v_max3_f32 v100, v100, v96, v97
	v_max3_f32 v100, v100, v66, v67
	v_max3_f32 v100, v100, v68, v69
	v_max3_f32 v100, v100, v70, v71
	v_max3_f32 v100, v100, v72, v73
	v_max3_f32 v100, v100, v74, v75
	v_max3_f32 v100, v100, v76, v77
	v_mfma_f32_32x32x16_bf16 v[18:33], v[118:121], v[138:141], v[18:33]
	v_max3_f32 v100, v100, v78, v79
	v_max3_f32 v100, v100, v80, v81
	v_mov_b32_e32 v101, v100
	s_nop 1
	v_permlane32_swap_b32_e32 v100, v101
	v_max_f32_e32 v101, v101, v101
	v_max_f32_e32 v100, v100, v100
	v_max_f32_e32 v100, v100, v101
	v_max_f32_e32 v101, v193, v193
	v_max_f32_e32 v101, v101, v100
	v_sub_f32_e32 v102, v100, v193
	v_mfma_f32_32x32x16_bf16 v[18:33], v[108:111], v[142:145], v[18:33]
	v_sub_f32_e32 v100, v193, v101
	v_mul_f32_e32 v100, 0x3e0293ee, v100
	v_exp_f32_e32 v100, v100
	v_cmp_ge_f32_e32 vcc, s89, v102
	s_cmp_eq_u64 vcc, exec
	s_cselect_b64 s[4:5], -1, 0
	v_cndmask_b32_e64 v100, v100, 1.0, s[4:5]
	v_cmp_gt_f32_e32 vcc, 1.0, v100
	s_cbranch_vccz .LBB0_433
	s_and_saveexec_b64 s[6:7], s[2:3]
	v_readlane_b32 s96, v250, 4
	v_readlane_b32 s97, v250, 5
	ds_write_b32 v180, v100 offset:128
	s_or_b64 exec, exec, s[6:7]
	s_waitcnt lgkmcnt(0)
	v_add_u32_e32 v114, v165, v166
	ds_read_b128 v[102:105], v114 offset:224
	ds_read_b128 v[106:109], v114 offset:192
	ds_read_b128 v[110:113], v114 offset:160
	ds_read_b128 v[114:117], v114 offset:128
	s_waitcnt lgkmcnt(0)
	v_pk_mul_f32 v[14:15], v[14:15], v[102:103]
	v_pk_mul_f32 v[10:11], v[10:11], v[106:107]
	v_pk_mul_f32 v[6:7], v[6:7], v[110:111]
	v_pk_mul_f32 v[16:17], v[16:17], v[104:105]
	v_pk_mul_f32 v[12:13], v[12:13], v[108:109]
	v_pk_mul_f32 v[8:9], v[8:9], v[112:113]
	v_pk_mul_f32 v[4:5], v[4:5], v[116:117]
	v_pk_mul_f32 v[2:3], v[2:3], v[114:115]
	v_pk_mul_f32 v[62:63], v[62:63], v[102:103]
	v_pk_mul_f32 v[58:59], v[58:59], v[106:107]
	v_pk_mul_f32 v[54:55], v[54:55], v[110:111]
	v_pk_mul_f32 v[64:65], v[64:65], v[104:105]
	v_pk_mul_f32 v[60:61], v[60:61], v[108:109]
	v_pk_mul_f32 v[56:57], v[56:57], v[112:113]
	v_pk_mul_f32 v[52:53], v[52:53], v[116:117]
	v_pk_mul_f32 v[50:51], v[50:51], v[114:115]
	v_pk_mul_f32 v[46:47], v[46:47], v[102:103]
	v_pk_mul_f32 v[42:43], v[42:43], v[106:107]
	v_pk_mul_f32 v[38:39], v[38:39], v[110:111]
	v_pk_mul_f32 v[48:49], v[48:49], v[104:105]
	v_pk_mul_f32 v[44:45], v[44:45], v[108:109]
	v_pk_mul_f32 v[40:41], v[40:41], v[112:113]
	v_pk_mul_f32 v[36:37], v[36:37], v[116:117]
	v_pk_mul_f32 v[34:35], v[34:35], v[114:115]
	v_pk_mul_f32 v[30:31], v[30:31], v[102:103]
	v_pk_mul_f32 v[26:27], v[26:27], v[106:107]
	v_pk_mul_f32 v[22:23], v[22:23], v[110:111]
	v_pk_mul_f32 v[32:33], v[32:33], v[104:105]
	v_pk_mul_f32 v[28:29], v[28:29], v[108:109]
	v_pk_mul_f32 v[24:25], v[24:25], v[112:113]
	v_pk_mul_f32 v[20:21], v[20:21], v[116:117]
	v_pk_mul_f32 v[18:19], v[18:19], v[114:115]
	s_branch .LBB0_434

; #define SBAR() __builtin_amdgcn_sched_barrier(0)
; __device__ __forceinline__ void finishSM(f32x16& p0, f32x16& p1, float alpha, float& l_reg, bf16x8& pa0, bf16x8& pa1, bf16x8& pa2, bf16x8& pa3) {
;   for (int r = 0; r < 16; ++r) p1[r] = __builtin_amdgcn_exp2f(p1[r]);
;   float ps = 0; for (int r = 0; r < 16; ++r) ps += p0[r]; for (int r = 0; r < 16; ++r) ps += p1[r];
;   { auto rr = __builtin_amdgcn_permlane32_swap(__float_as_uint(ps), __float_as_uint(ps), false, false);
;     ps = __uint_as_float(rr[0]) + __uint_as_float(rr[1]); }
;   l_reg = l_reg * alpha + ps;
;     ...
;   PK4(p0, 0, pa0); PK4(p0, 8, pa1); PK4(p1, 0, pa2); PK4(p1, 8, pa3);
;     ...
; }
; __device__ __forceinline__ void attn_dma_body(const bf16_t* __restrict__ Qb, int ldq, int tpos0, const float* __restrict__ rope, const float* __restrict__ qgain, ...
;     ...
;     finishSM(pB0, pB1, alB, l_reg, pa0, pa1, pa2, pa3); SBAR();
;     pv_d0(o, vb0 + ((NT - 1) & 3) * (int)SHM_SLOT, pa0, pa1, pa2, pa3); }
.LBB0_434:
	v_cndmask_b32_e64 v101, v101, v193, s[4:5]
	v_mul_f32_e32 v101, 0xbe0293ee, v101
	v_fmamk_f32 v82, v82, 0x3e0293ee, v101
	v_fmamk_f32 v83, v83, 0x3e0293ee, v101
	v_fmamk_f32 v84, v84, 0x3e0293ee, v101
	v_fmamk_f32 v85, v85, 0x3e0293ee, v101
	v_fmamk_f32 v86, v86, 0x3e0293ee, v101
	v_fmamk_f32 v87, v87, 0x3e0293ee, v101
	v_fmamk_f32 v88, v88, 0x3e0293ee, v101
	v_fmamk_f32 v89, v89, 0x3e0293ee, v101
	v_fmamk_f32 v90, v90, 0x3e0293ee, v101
	v_fmamk_f32 v91, v91, 0x3e0293ee, v101
	v_fmamk_f32 v92, v92, 0x3e0293ee, v101
	v_fmamk_f32 v93, v93, 0x3e0293ee, v101
	v_fmamk_f32 v94, v94, 0x3e0293ee, v101
	v_fmamk_f32 v95, v95, 0x3e0293ee, v101
	v_fmamk_f32 v96, v96, 0x3e0293ee, v101
	v_fmamk_f32 v97, v97, 0x3e0293ee, v101
	v_fmamk_f32 v66, v66, 0x3e0293ee, v101
	v_fmamk_f32 v67, v67, 0x3e0293ee, v101
	v_fmamk_f32 v68, v68, 0x3e0293ee, v101
	v_fmamk_f32 v69, v69, 0x3e0293ee, v101
	v_fmamk_f32 v70, v70, 0x3e0293ee, v101
	v_fmamk_f32 v71, v71, 0x3e0293ee, v101
	v_fmamk_f32 v72, v72, 0x3e0293ee, v101
	v_fmamk_f32 v73, v73, 0x3e0293ee, v101
	v_fmamk_f32 v74, v74, 0x3e0293ee, v101
	v_fmamk_f32 v75, v75, 0x3e0293ee, v101
	v_fmamk_f32 v76, v76, 0x3e0293ee, v101
	v_fmamk_f32 v77, v77, 0x3e0293ee, v101
	v_fmamk_f32 v78, v78, 0x3e0293ee, v101
	v_fmamk_f32 v79, v79, 0x3e0293ee, v101
	v_fmamk_f32 v80, v80, 0x3e0293ee, v101
	v_fmac_f32_e32 v101, 0x3e0293ee, v81
	v_exp_f32_e32 v81, v82
	v_exp_f32_e32 v82, v83
	v_exp_f32_e32 v83, v84
	v_exp_f32_e32 v84, v85
	v_exp_f32_e32 v85, v86
	v_exp_f32_e32 v86, v87
	v_exp_f32_e32 v87, v88
	v_exp_f32_e32 v88, v89
	v_exp_f32_e32 v89, v90
	v_exp_f32_e32 v90, v91
	v_exp_f32_e32 v91, v92
	v_exp_f32_e32 v92, v93
	v_exp_f32_e32 v93, v94
	v_exp_f32_e32 v94, v95
	v_exp_f32_e32 v95, v96
	v_exp_f32_e32 v96, v97
	v_exp_f32_e32 v97, v66
	v_add_f32_e32 v66, 0, v81
	v_add_f32_e32 v66, v82, v66
	v_add_f32_e32 v66, v83, v66
	v_add_f32_e32 v66, v84, v66
	v_add_f32_e32 v66, v85, v66
	v_add_f32_e32 v66, v86, v66
	v_add_f32_e32 v66, v87, v66
	v_add_f32_e32 v66, v88, v66
	v_add_f32_e32 v66, v89, v66
	v_add_f32_e32 v66, v90, v66
	v_add_f32_e32 v66, v91, v66
	v_add_f32_e32 v66, v92, v66
	v_add_f32_e32 v66, v93, v66
	v_exp_f32_e32 v102, v67
	v_add_f32_e32 v66, v94, v66
	v_exp_f32_e32 v103, v68
	v_add_f32_e32 v66, v95, v66
	v_exp_f32_e32 v104, v69
	v_add_f32_e32 v66, v96, v66
	v_exp_f32_e32 v105, v70
	v_add_f32_e32 v66, v97, v66
	v_exp_f32_e32 v106, v71
	v_add_f32_e32 v66, v102, v66
	v_exp_f32_e32 v107, v72
	v_add_f32_e32 v66, v103, v66
	v_exp_f32_e32 v108, v73
	v_add_f32_e32 v66, v104, v66
	v_exp_f32_e32 v109, v74
	v_add_f32_e32 v66, v105, v66
	v_exp_f32_e32 v110, v75
	v_add_f32_e32 v66, v106, v66
	v_exp_f32_e32 v111, v76
	v_add_f32_e32 v66, v107, v66
	v_exp_f32_e32 v112, v77
	v_add_f32_e32 v66, v108, v66
	v_exp_f32_e32 v113, v78
	v_add_f32_e32 v66, v109, v66
	v_exp_f32_e32 v114, v79
	v_add_f32_e32 v66, v110, v66
	v_exp_f32_e32 v115, v80
	v_add_f32_e32 v66, v111, v66
	v_exp_f32_e32 v101, v101
	v_add_f32_e32 v66, v112, v66
	v_add_f32_e32 v66, v113, v66
	v_add_f32_e32 v66, v114, v66
	v_add_f32_e32 v66, v115, v66
	v_add_f32_e32 v66, v101, v66
	v_mov_b32_e32 v67, v66
	s_nop 1
	v_permlane32_swap_b32_e32 v66, v67
	v_cvt_pk_bf16_f32 v68, v81, v82
	v_cvt_pk_bf16_f32 v69, v83, v84
	v_cvt_pk_bf16_f32 v70, v85, v86
	v_cvt_pk_bf16_f32 v71, v87, v88
	v_cvt_pk_bf16_f32 v72, v89, v90
	v_cvt_pk_bf16_f32 v73, v91, v92
	v_cvt_pk_bf16_f32 v74, v93, v94
	v_cvt_pk_bf16_f32 v75, v95, v96
	v_cvt_pk_bf16_f32 v76, v97, v102
	v_cvt_pk_bf16_f32 v77, v103, v104
	v_cvt_pk_bf16_f32 v78, v105, v106
	v_cvt_pk_bf16_f32 v79, v107, v108
	v_cvt_pk_bf16_f32 v80, v109, v110
	v_cvt_pk_bf16_f32 v81, v111, v112
	v_cvt_pk_bf16_f32 v82, v113, v114
	v_cvt_pk_bf16_f32 v83, v115, v101
	s_nop 0
	s_cmp_lg_u32 0, -1
	s_cselect_b32 s4, 0, 0
	s_add_i32 s4, s4, 0x1c000
	v_add_u32_e32 v96, s4, v181
	ds_read_b64_tr_b16 v[84:85], v96 offset:0
	ds_read_b64_tr_b16 v[86:87], v96 offset:0x800
	ds_read_b64_tr_b16 v[88:89], v96 offset:0x1000
	ds_read_b64_tr_b16 v[90:91], v96 offset:0x1800
	ds_read_b64_tr_b16 v[92:93], v96 offset:0x2000
	ds_read_b64_tr_b16 v[94:95], v96 offset:0x2800
	ds_read_b64_tr_b16 v[102:103], v96 offset:0x3000
	ds_read_b64_tr_b16 v[104:105], v96 offset:0x3800
	ds_read_b64_tr_b16 v[106:107], v96 offset:0x200
	ds_read_b64_tr_b16 v[108:109], v96 offset:0xa00
	ds_read_b64_tr_b16 v[110:111], v96 offset:0x1200
	ds_read_b64_tr_b16 v[112:113], v96 offset:0x1a00
	ds_read_b64_tr_b16 v[114:115], v96 offset:0x2200
	ds_read_b64_tr_b16 v[116:117], v96 offset:0x2a00
	ds_read_b64_tr_b16 v[118:119], v96 offset:0x3200
	ds_read_b64_tr_b16 v[120:121], v96 offset:0x3a00
	s_waitcnt lgkmcnt(8)
	s_nop 0
	v_mfma_f32_32x32x16_bf16 v[2:17], v[68:71], v[84:87], v[2:17]
	ds_read_b64_tr_b16 v[84:85], v96 offset:0x400
	ds_read_b64_tr_b16 v[86:87], v96 offset:0xc00
	v_mfma_f32_32x32x16_bf16 v[2:17], v[72:75], v[88:91], v[2:17]
	ds_read_b64_tr_b16 v[88:89], v96 offset:0x1400
	ds_read_b64_tr_b16 v[90:91], v96 offset:0x1c00
	v_mfma_f32_32x32x16_bf16 v[2:17], v[76:79], v[92:95], v[2:17]
	ds_read_b64_tr_b16 v[92:93], v96 offset:0x2400
	ds_read_b64_tr_b16 v[94:95], v96 offset:0x2c00
	ds_read_b64_tr_b16 v[122:123], v96 offset:0x3400
	ds_read_b64_tr_b16 v[124:125], v96 offset:0x3c00
	s_waitcnt lgkmcnt(8)
	v_mfma_f32_32x32x16_bf16 v[2:17], v[80:83], v[102:105], v[2:17]
	v_mfma_f32_32x32x16_bf16 v[50:65], v[68:71], v[106:109], v[50:65]
	ds_read_b64_tr_b16 v[102:103], v96 offset:0x600
	ds_read_b64_tr_b16 v[104:105], v96 offset:0xe00
	ds_read_b64_tr_b16 v[106:107], v96 offset:0x1600
	ds_read_b64_tr_b16 v[108:109], v96 offset:0x1e00
	v_mfma_f32_32x32x16_bf16 v[50:65], v[72:75], v[110:113], v[50:65]
	ds_read_b64_tr_b16 v[110:111], v96 offset:0x2600
	ds_read_b64_tr_b16 v[112:113], v96 offset:0x2e00
	v_mfma_f32_32x32x16_bf16 v[50:65], v[76:79], v[114:117], v[50:65]
	ds_read_b64_tr_b16 v[114:115], v96 offset:0x3600
	ds_read_b64_tr_b16 v[116:117], v96 offset:0x3e00
	s_waitcnt lgkmcnt(8)
; __device__ __forceinline__ unsigned f2bf(float f) { unsigned u = __builtin_bit_cast(unsigned, f); return (u + 0x7fffu + ((u >> 16) & 1u)) >> 16; }
; __device__ __forceinline__ int crow(int r, int hi) { return (r & 3) + 8 * (r >> 2) + 4 * hi; }
; __device__ __forceinline__ void attn_dma_body(const bf16_t* __restrict__ Qb, int ldq, int tpos0, const float* __restrict__ rope, const float* __restrict__ qgain, ...
;     ...
;   if (hi == 0) li_l[r32] = l_reg; asm volatile("s_waitcnt lgkmcnt(0)" ::: "memory");
;   float rli[16];
; #pragma unroll
;   for (int r = 0; r < 16; ++r) rli[r] = __builtin_amdgcn_rcpf(li_l[crow(r, hi)]);
;   bf16_t* Ow = Ob + (long)(wid * QBLK) * LDO;
;   asm volatile("s_waitcnt lgkmcnt(0)\n\ts_barrier" ::: "memory");
;   { char* st = lds + wid * 8704;
; #pragma unroll
;     for (int r = 0; r < 16; ++r) { const int orow = crow(r, hi);
; #pragma unroll
;       for (int d0 = 0; d0 < 4; ++d0) *(bf16_t*)(st + orow * 272 + (d0 * 32 + r32) * 2) = (bf16_t)f2bf(o[d0][r] * rli[r]); }
;     asm volatile("s_waitcnt lgkmcnt(0)" ::: "memory");
	v_mfma_f32_32x32x16_bf16 v[50:65], v[80:83], v[118:121], v[50:65]
	v_mfma_f32_32x32x16_bf16 v[34:49], v[68:71], v[84:87], v[34:49]
	s_waitcnt lgkmcnt(0)
	v_mfma_f32_32x32x16_bf16 v[34:49], v[72:75], v[88:91], v[34:49]
	v_mfma_f32_32x32x16_bf16 v[34:49], v[76:79], v[92:95], v[34:49]
	v_mfma_f32_32x32x16_bf16 v[34:49], v[80:83], v[122:125], v[34:49]
	v_mfma_f32_32x32x16_bf16 v[18:33], v[68:71], v[102:105], v[18:33]
	v_mfma_f32_32x32x16_bf16 v[18:33], v[72:75], v[106:109], v[18:33]
	v_mfma_f32_32x32x16_bf16 v[18:33], v[76:79], v[110:113], v[18:33]
	v_mfma_f32_32x32x16_bf16 v[18:33], v[80:83], v[114:117], v[18:33]
	s_and_saveexec_b64 s[4:5], s[2:3]
	v_add_f32_e32 v68, v98, v99
	v_fmac_f32_e32 v68, v182, v146
	v_add_f32_e32 v66, v66, v67
	v_fmac_f32_e32 v66, v68, v100
	ds_write_b32 v180, v66
	s_or_b64 exec, exec, s[4:5]
	s_waitcnt lgkmcnt(0)
	v_add_u32_e32 v74, v165, v166
	ds_read_b128 v[66:69], v74
	ds_read_b128 v[70:73], v74 offset:32
	v_mul_lo_u32 v84, v179, s91
	v_add_u32_e32 v84, 0, v84
	v_lshlrev_b32_e32 v85, 1, v177
	s_waitcnt lgkmcnt(0)
	v_rcp_f32_e32 v75, v66
	v_mul_u32_u24_e32 v86, 0x440, v178
	v_add3_u32 v85, v84, v85, v86
	v_rcp_f32_e32 v76, v67
	v_mul_f32_e32 v2, v2, v75
	v_bfe_u32 v86, v2, 16, 1
	v_add3_u32 v2, v2, v86, s92
	v_rcp_f32_e32 v77, v68
	v_rcp_f32_e32 v78, v69
	v_rcp_f32_e32 v79, v70
	ds_read_b128 v[66:69], v74 offset:64
	v_rcp_f32_e32 v80, v71
	v_rcp_f32_e32 v81, v72
	v_rcp_f32_e32 v82, v73
	ds_read_b128 v[70:73], v74 offset:96
	s_waitcnt lgkmcnt(0)
	s_barrier
	ds_write_b16_d16_hi v85, v2
	v_mul_f32_e32 v2, v50, v75
	v_bfe_u32 v50, v2, 16, 1
	v_add3_u32 v2, v2, v50, s92
	ds_write_b16_d16_hi v85, v2 offset:64
	v_mul_f32_e32 v2, v34, v75
	v_bfe_u32 v34, v2, 16, 1
	v_add3_u32 v2, v2, v34, s92
	ds_write_b16_d16_hi v85, v2 offset:128
	v_mul_f32_e32 v2, v18, v75
	v_bfe_u32 v18, v2, 16, 1
	v_add3_u32 v2, v2, v18, s92
	ds_write_b16_d16_hi v85, v2 offset:192
	v_mul_f32_e32 v2, v3, v76
	v_bfe_u32 v3, v2, 16, 1
	v_add3_u32 v2, v2, v3, s92
	ds_write_b16_d16_hi v85, v2 offset:272
	v_mul_f32_e32 v2, v51, v76
	v_bfe_u32 v3, v2, 16, 1
	v_add3_u32 v2, v2, v3, s92
	ds_write_b16_d16_hi v85, v2 offset:336
	v_mul_f32_e32 v2, v35, v76
	v_bfe_u32 v3, v2, 16, 1
	v_add3_u32 v2, v2, v3, s92
	ds_write_b16_d16_hi v85, v2 offset:400
	v_mul_f32_e32 v2, v19, v76
	v_bfe_u32 v3, v2, 16, 1
	v_add3_u32 v2, v2, v3, s92
	ds_write_b16_d16_hi v85, v2 offset:464
	v_mul_f32_e32 v2, v4, v77
	v_bfe_u32 v3, v2, 16, 1
	v_add3_u32 v2, v2, v3, s92
	ds_write_b16_d16_hi v85, v2 offset:544
	v_mul_f32_e32 v2, v52, v77
	v_bfe_u32 v3, v2, 16, 1
	v_add3_u32 v2, v2, v3, s92
	ds_write_b16_d16_hi v85, v2 offset:608
	v_mul_f32_e32 v2, v36, v77
	v_bfe_u32 v3, v2, 16, 1
	v_add3_u32 v2, v2, v3, s92
	ds_write_b16_d16_hi v85, v2 offset:672
	v_mul_f32_e32 v2, v20, v77
	v_bfe_u32 v3, v2, 16, 1
	v_add3_u32 v2, v2, v3, s92
	ds_write_b16_d16_hi v85, v2 offset:736
	v_mul_f32_e32 v2, v5, v78
	v_bfe_u32 v3, v2, 16, 1
	v_add3_u32 v2, v2, v3, s92
	ds_write_b16_d16_hi v85, v2 offset:816
	v_mul_f32_e32 v2, v53, v78
	v_bfe_u32 v3, v2, 16, 1
	v_add3_u32 v2, v2, v3, s92
	ds_write_b16_d16_hi v85, v2 offset:880
	v_mul_f32_e32 v2, v37, v78
	v_bfe_u32 v3, v2, 16, 1
	v_add3_u32 v2, v2, v3, s92
	ds_write_b16_d16_hi v85, v2 offset:944
	v_mul_f32_e32 v2, v21, v78
	v_bfe_u32 v3, v2, 16, 1
	v_add3_u32 v2, v2, v3, s92
	ds_write_b16_d16_hi v85, v2 offset:1008
	v_mul_f32_e32 v2, v6, v79
	v_bfe_u32 v3, v2, 16, 1
	v_add3_u32 v2, v2, v3, s92
	ds_write_b16_d16_hi v85, v2 offset:2176
	v_mul_f32_e32 v2, v54, v79
	v_bfe_u32 v3, v2, 16, 1
	v_add3_u32 v2, v2, v3, s92
	ds_write_b16_d16_hi v85, v2 offset:2240
	v_mul_f32_e32 v2, v38, v79
	v_bfe_u32 v3, v2, 16, 1
	v_add3_u32 v2, v2, v3, s92
	ds_write_b16_d16_hi v85, v2 offset:2304
	v_mul_f32_e32 v2, v22, v79
	v_bfe_u32 v3, v2, 16, 1
	v_add3_u32 v2, v2, v3, s92
	ds_write_b16_d16_hi v85, v2 offset:2368
	v_mul_f32_e32 v2, v7, v80
	v_bfe_u32 v3, v2, 16, 1
	v_add3_u32 v2, v2, v3, s92
	ds_write_b16_d16_hi v85, v2 offset:2448
	v_mul_f32_e32 v2, v55, v80
	v_bfe_u32 v3, v2, 16, 1
	v_add3_u32 v2, v2, v3, s92
	ds_write_b16_d16_hi v85, v2 offset:2512
	v_mul_f32_e32 v2, v39, v80
	v_bfe_u32 v3, v2, 16, 1
	v_add3_u32 v2, v2, v3, s92
	ds_write_b16_d16_hi v85, v2 offset:2576
	v_mul_f32_e32 v2, v23, v80
	v_bfe_u32 v3, v2, 16, 1
	v_add3_u32 v2, v2, v3, s92
	ds_write_b16_d16_hi v85, v2 offset:2640
	v_mul_f32_e32 v2, v8, v81
	v_bfe_u32 v3, v2, 16, 1
	v_add3_u32 v2, v2, v3, s92
	ds_write_b16_d16_hi v85, v2 offset:2720
	v_mul_f32_e32 v2, v56, v81
	v_bfe_u32 v3, v2, 16, 1
	v_add3_u32 v2, v2, v3, s92
	ds_write_b16_d16_hi v85, v2 offset:2784
	v_mul_f32_e32 v2, v40, v81
	v_bfe_u32 v3, v2, 16, 1
	v_add3_u32 v2, v2, v3, s92
	ds_write_b16_d16_hi v85, v2 offset:2848
	v_mul_f32_e32 v2, v24, v81
	v_bfe_u32 v3, v2, 16, 1
	v_add3_u32 v2, v2, v3, s92
	ds_write_b16_d16_hi v85, v2 offset:2912
	v_mul_f32_e32 v2, v9, v82
	v_bfe_u32 v3, v2, 16, 1
	v_add3_u32 v2, v2, v3, s92
	ds_write_b16_d16_hi v85, v2 offset:2992
	v_mul_f32_e32 v2, v57, v82
	v_bfe_u32 v3, v2, 16, 1
	v_add3_u32 v2, v2, v3, s92
	ds_write_b16_d16_hi v85, v2 offset:3056
	v_mul_f32_e32 v2, v41, v82
	v_bfe_u32 v3, v2, 16, 1
	s_waitcnt lgkmcnt(0)
; __device__ __forceinline__ unsigned f2bf(float f) { unsigned u = __builtin_bit_cast(unsigned, f); return (u + 0x7fffu + ((u >> 16) & 1u)) >> 16; }
; __device__ __forceinline__ int crow(int r, int hi) { return (r & 3) + 8 * (r >> 2) + 4 * hi; }
; #define ATT_WAIT_BAR() asm volatile("s_waitcnt vmcnt(0) lgkmcnt(0)\n\ts_barrier" ::: "memory")
; __device__ __forceinline__ void attn_dma_body(const bf16_t* __restrict__ Qb, int ldq, int tpos0, const float* __restrict__ rope, const float* __restrict__ qgain, ...
;     ...
;   { char* st = lds + wid * 8704;
; #pragma unroll
;     for (int r = 0; r < 16; ++r) { const int orow = crow(r, hi);
; #pragma unroll
;       for (int d0 = 0; d0 < 4; ++d0) *(bf16_t*)(st + orow * 272 + (d0 * 32 + r32) * 2) = (bf16_t)f2bf(o[d0][r] * rli[r]); }
;     asm volatile("s_waitcnt lgkmcnt(0)" ::: "memory");
; #pragma unroll
;     for (int i = 0; i < 8; ++i) { const int c = i * 64 + lane, row = c >> 4, cc = c & 15; const u32x4 v = *(const u32x4*)(st + row * 272 + cc * 16);
;       const bf16_t* gp = Ow + (long)row * LDO + cc * 8;
;       asm volatile("global_store_dwordx4 %0, %1, off sc1\n\ts_nop 1" :: "v"(gp), "v"(v) : "memory"); } }
;   ATT_WAIT_BAR();
	v_rcp_f32_e32 v74, v66
	v_add3_u32 v2, v2, v3, s92
	ds_write_b16_d16_hi v85, v2 offset:3120
	v_mul_f32_e32 v2, v25, v82
	v_bfe_u32 v3, v2, 16, 1
	v_add3_u32 v2, v2, v3, s92
	ds_write_b16_d16_hi v85, v2 offset:3184
	v_mul_f32_e32 v2, v10, v74
	v_bfe_u32 v3, v2, 16, 1
	v_add3_u32 v2, v2, v3, s92
	ds_write_b16_d16_hi v85, v2 offset:4352
	v_mul_f32_e32 v2, v58, v74
	v_bfe_u32 v3, v2, 16, 1
	v_add3_u32 v2, v2, v3, s92
	ds_write_b16_d16_hi v85, v2 offset:4416
	v_mul_f32_e32 v2, v42, v74
	v_bfe_u32 v3, v2, 16, 1
	v_rcp_f32_e32 v83, v67
	v_add3_u32 v2, v2, v3, s92
	ds_write_b16_d16_hi v85, v2 offset:4480
	v_mul_f32_e32 v2, v26, v74
	v_bfe_u32 v3, v2, 16, 1
	v_add3_u32 v2, v2, v3, s92
	ds_write_b16_d16_hi v85, v2 offset:4544
	v_mul_f32_e32 v2, v11, v83
	v_bfe_u32 v3, v2, 16, 1
	v_add3_u32 v2, v2, v3, s92
	ds_write_b16_d16_hi v85, v2 offset:4624
	v_mul_f32_e32 v2, v59, v83
	v_bfe_u32 v3, v2, 16, 1
	v_add3_u32 v2, v2, v3, s92
	ds_write_b16_d16_hi v85, v2 offset:4688
	v_mul_f32_e32 v2, v43, v83
	v_bfe_u32 v3, v2, 16, 1
	v_rcp_f32_e32 v68, v68
	v_add3_u32 v2, v2, v3, s92
	ds_write_b16_d16_hi v85, v2 offset:4752
	v_mul_f32_e32 v2, v27, v83
	v_bfe_u32 v3, v2, 16, 1
	v_add3_u32 v2, v2, v3, s92
	ds_write_b16_d16_hi v85, v2 offset:4816
	v_mul_f32_e32 v2, v12, v68
	v_bfe_u32 v3, v2, 16, 1
	v_add3_u32 v2, v2, v3, s92
	ds_write_b16_d16_hi v85, v2 offset:4896
	v_mul_f32_e32 v2, v60, v68
	v_bfe_u32 v3, v2, 16, 1
	v_add3_u32 v2, v2, v3, s92
	ds_write_b16_d16_hi v85, v2 offset:4960
	v_mul_f32_e32 v2, v44, v68
	v_bfe_u32 v3, v2, 16, 1
	v_rcp_f32_e32 v69, v69
	v_add3_u32 v2, v2, v3, s92
	ds_write_b16_d16_hi v85, v2 offset:5024
	v_mul_f32_e32 v2, v28, v68
	v_bfe_u32 v3, v2, 16, 1
	v_add3_u32 v2, v2, v3, s92
	ds_write_b16_d16_hi v85, v2 offset:5088
	v_mul_f32_e32 v2, v13, v69
	v_bfe_u32 v3, v2, 16, 1
	v_add3_u32 v2, v2, v3, s92
	ds_write_b16_d16_hi v85, v2 offset:5168
	v_mul_f32_e32 v2, v61, v69
	v_bfe_u32 v3, v2, 16, 1
	v_add3_u32 v2, v2, v3, s92
	ds_write_b16_d16_hi v85, v2 offset:5232
	v_mul_f32_e32 v2, v45, v69
	v_bfe_u32 v3, v2, 16, 1
	v_rcp_f32_e32 v70, v70
	v_add3_u32 v2, v2, v3, s92
	ds_write_b16_d16_hi v85, v2 offset:5296
	v_mul_f32_e32 v2, v29, v69
	v_bfe_u32 v3, v2, 16, 1
	v_add3_u32 v2, v2, v3, s92
	ds_write_b16_d16_hi v85, v2 offset:5360
	v_mul_f32_e32 v2, v14, v70
	v_bfe_u32 v3, v2, 16, 1
	v_add3_u32 v2, v2, v3, s92
	ds_write_b16_d16_hi v85, v2 offset:6528
	v_mul_f32_e32 v2, v62, v70
	v_bfe_u32 v3, v2, 16, 1
	v_add3_u32 v2, v2, v3, s92
	ds_write_b16_d16_hi v85, v2 offset:6592
	v_mul_f32_e32 v2, v46, v70
	v_bfe_u32 v3, v2, 16, 1
	v_rcp_f32_e32 v71, v71
	v_add3_u32 v2, v2, v3, s92
	ds_write_b16_d16_hi v85, v2 offset:6656
	v_mul_f32_e32 v2, v30, v70
	v_bfe_u32 v3, v2, 16, 1
	v_add3_u32 v2, v2, v3, s92
	ds_write_b16_d16_hi v85, v2 offset:6720
	v_mul_f32_e32 v2, v15, v71
	v_bfe_u32 v3, v2, 16, 1
	v_add3_u32 v2, v2, v3, s92
	ds_write_b16_d16_hi v85, v2 offset:6800
	v_mul_f32_e32 v2, v63, v71
	v_bfe_u32 v3, v2, 16, 1
	v_add3_u32 v2, v2, v3, s92
	ds_write_b16_d16_hi v85, v2 offset:6864
	v_mul_f32_e32 v2, v47, v71
	v_bfe_u32 v3, v2, 16, 1
	v_rcp_f32_e32 v72, v72
	v_add3_u32 v2, v2, v3, s92
	ds_write_b16_d16_hi v85, v2 offset:6928
	v_mul_f32_e32 v2, v31, v71
	v_bfe_u32 v3, v2, 16, 1
	v_add3_u32 v2, v2, v3, s92
	ds_write_b16_d16_hi v85, v2 offset:6992
	v_mul_f32_e32 v2, v16, v72
	v_bfe_u32 v3, v2, 16, 1
	v_add3_u32 v2, v2, v3, s92
	ds_write_b16_d16_hi v85, v2 offset:7072
	v_mul_f32_e32 v2, v64, v72
	v_bfe_u32 v3, v2, 16, 1
	v_add3_u32 v2, v2, v3, s92
	ds_write_b16_d16_hi v85, v2 offset:7136
	v_mul_f32_e32 v2, v48, v72
	v_bfe_u32 v3, v2, 16, 1
	v_rcp_f32_e32 v73, v73
	v_add3_u32 v2, v2, v3, s92
	ds_write_b16_d16_hi v85, v2 offset:7200
	v_mul_f32_e32 v2, v32, v72
	v_bfe_u32 v3, v2, 16, 1
	v_add3_u32 v2, v2, v3, s92
	ds_write_b16_d16_hi v85, v2 offset:7264
	v_mul_f32_e32 v2, v17, v73
	v_bfe_u32 v3, v2, 16, 1
	v_add3_u32 v2, v2, v3, s92
	ds_write_b16_d16_hi v85, v2 offset:7344
	v_mul_f32_e32 v2, v65, v73
	v_bfe_u32 v3, v2, 16, 1
	v_add3_u32 v2, v2, v3, s92
	ds_write_b16_d16_hi v85, v2 offset:7408
	v_mul_f32_e32 v2, v49, v73
	s_lshl_b64 s[2:3], s[70:71], 12
	v_bfe_u32 v3, v2, 16, 1
	s_add_u32 s2, s23, s2
	v_add3_u32 v2, v2, v3, s92
	s_addc_u32 s3, s94, s3
	ds_write_b16_d16_hi v85, v2 offset:7472
	v_mul_f32_e32 v2, v33, v73
	s_add_u32 s2, s2, s44
	v_ashrrev_i32_e32 v165, 31, v164
	v_bfe_u32 v3, v2, 16, 1
	s_addc_u32 s3, s3, s45
	v_lshlrev_b64 v[66:67], 12, v[164:165]
	v_add3_u32 v2, v2, v3, s92
	v_lshrrev_b32_e32 v8, 4, v167
	ds_write_b16_d16_hi v85, v2 offset:7536
	v_lshlrev_b32_e32 v162, 4, v176
	v_mul_u32_u24_e32 v2, 0x110, v8
	v_lshl_add_u64 v[6:7], s[2:3], 0, v[66:67]
	v_add3_u32 v10, v84, v162, v2
	v_lshl_add_u64 v[6:7], v[6:7], 0, v[162:163]
	v_lshlrev_b32_e32 v162, 12, v8
	s_waitcnt lgkmcnt(0)
	v_lshl_add_u64 v[8:9], v[6:7], 0, v[162:163]
	ds_read_b128 v[2:5], v10
	s_waitcnt lgkmcnt(0)
	global_store_dwordx4 v[8:9], v[2:5], off sc1
	s_nop 1
	v_or_b32_e32 v8, 0x4000, v162
	v_mov_b32_e32 v9, v163
	v_lshl_add_u64 v[8:9], v[6:7], 0, v[8:9]
	ds_read_b128 v[2:5], v10 offset:1088
	s_waitcnt lgkmcnt(0)
	global_store_dwordx4 v[8:9], v[2:5], off sc1
	s_nop 1
	v_or_b32_e32 v8, 0x8000, v162
	v_mov_b32_e32 v9, v163
	v_lshl_add_u64 v[8:9], v[6:7], 0, v[8:9]
	ds_read_b128 v[2:5], v10 offset:2176
	s_waitcnt lgkmcnt(0)
	global_store_dwordx4 v[8:9], v[2:5], off sc1
	s_nop 1
	v_or_b32_e32 v8, 0xc000, v162
	v_mov_b32_e32 v9, v163
	v_lshl_add_u64 v[8:9], v[6:7], 0, v[8:9]
	ds_read_b128 v[2:5], v10 offset:3264
	s_waitcnt lgkmcnt(0)
	global_store_dwordx4 v[8:9], v[2:5], off sc1
	s_nop 1
	v_or_b32_e32 v8, 0x10000, v162
	v_mov_b32_e32 v9, v163
	v_lshl_add_u64 v[8:9], v[6:7], 0, v[8:9]
	ds_read_b128 v[2:5], v10 offset:4352
	s_waitcnt lgkmcnt(0)
	global_store_dwordx4 v[8:9], v[2:5], off sc1
	s_nop 1
	v_or_b32_e32 v8, 0x14000, v162
	v_mov_b32_e32 v9, v163
	v_lshl_add_u64 v[8:9], v[6:7], 0, v[8:9]
	ds_read_b128 v[2:5], v10 offset:5440
	s_waitcnt lgkmcnt(0)
	global_store_dwordx4 v[8:9], v[2:5], off sc1
	s_nop 1
	v_or_b32_e32 v8, 0x18000, v162
	v_mov_b32_e32 v9, v163
	ds_read_b128 v[2:5], v10 offset:6528
	v_lshl_add_u64 v[8:9], v[6:7], 0, v[8:9]
	s_waitcnt lgkmcnt(0)
	global_store_dwordx4 v[8:9], v[2:5], off sc1
	s_nop 1
	v_or_b32_e32 v162, 0x1c000, v162
	ds_read_b128 v[2:5], v10 offset:7616
	v_lshl_add_u64 v[6:7], v[6:7], 0, v[162:163]
	s_waitcnt lgkmcnt(0)
	global_store_dwordx4 v[6:7], v[2:5], off sc1
	s_nop 1
	s_waitcnt vmcnt(0) lgkmcnt(0)
	s_barrier

; __global__ void __launch_bounds__(512, 2) mk_fwd(Params p_unused) {
;     extern __shared__ __attribute__((aligned(16))) unsigned char lds[];
	.amdhsa_kernel _Z6mk_fwd6Params
		.amdhsa_group_segment_fixed_size 0
		.amdhsa_private_segment_fixed_size 0
		.amdhsa_kernarg_size 432
		.amdhsa_user_sgpr_count 2
		.amdhsa_user_sgpr_dispatch_ptr 0
		.amdhsa_user_sgpr_queue_ptr 0
		.amdhsa_user_sgpr_kernarg_segment_ptr 1
		.amdhsa_user_sgpr_dispatch_id 0
		.amdhsa_user_sgpr_kernarg_preload_length 0
		.amdhsa_user_sgpr_kernarg_preload_offset 0
		.amdhsa_user_sgpr_private_segment_size 0
		.amdhsa_uses_dynamic_stack 0
		.amdhsa_enable_private_segment 0
		.amdhsa_system_sgpr_workgroup_id_x 1
		.amdhsa_system_sgpr_workgroup_id_y 0
		.amdhsa_system_sgpr_workgroup_id_z 0
		.amdhsa_system_sgpr_workgroup_info 0
		.amdhsa_system_vgpr_workitem_id 0
		.amdhsa_next_free_vgpr 251
		.amdhsa_next_free_sgpr 102
		.amdhsa_accum_offset 252
		.amdhsa_reserve_vcc 1
		.amdhsa_float_round_mode_32 0
		.amdhsa_float_round_mode_16_64 0
		.amdhsa_float_denorm_mode_32 3
		.amdhsa_float_denorm_mode_16_64 3
		.amdhsa_dx10_clamp 1
		.amdhsa_ieee_mode 1
		.amdhsa_fp16_overflow 0
		.amdhsa_tg_split 0
		.amdhsa_exception_fp_ieee_invalid_op 0
		.amdhsa_exception_fp_denorm_src 0
		.amdhsa_exception_fp_ieee_div_zero 0
		.amdhsa_exception_fp_ieee_overflow 0
		.amdhsa_exception_fp_ieee_underflow 0
		.amdhsa_exception_fp_ieee_inexact 0
		.amdhsa_exception_int_div_zero 0
	.end_amdhsa_kernel

; __global__ void __launch_bounds__(512, 2) mk_fwd(Params p_unused) {
;     extern __shared__ __attribute__((aligned(16))) unsigned char lds[];
amdhsa.kernels:
  - .agpr_count:     0
    .args:
      - .offset:         0
        .size:           176
        .value_kind:     by_value
      - .offset:         176
        .size:           4
        .value_kind:     hidden_block_count_x
      - .offset:         180
        .size:           4
        .value_kind:     hidden_block_count_y
      - .offset:         184
        .size:           4
        .value_kind:     hidden_block_count_z
      - .offset:         188
        .size:           2
        .value_kind:     hidden_group_size_x
      - .offset:         190
        .size:           2
        .value_kind:     hidden_group_size_y
      - .offset:         192
        .size:           2
        .value_kind:     hidden_group_size_z
      - .offset:         194
        .size:           2
        .value_kind:     hidden_remainder_x
      - .offset:         196
        .size:           2
        .value_kind:     hidden_remainder_y
      - .offset:         198
        .size:           2
        .value_kind:     hidden_remainder_z
      - .offset:         216
        .size:           8
        .value_kind:     hidden_global_offset_x
      - .offset:         224
        .size:           8
        .value_kind:     hidden_global_offset_y
      - .offset:         232
        .size:           8
        .value_kind:     hidden_global_offset_z
      - .offset:         240
        .size:           2
        .value_kind:     hidden_grid_dims
      - .offset:         296
        .size:           4
        .value_kind:     hidden_dynamic_lds_size
    .group_segment_fixed_size: 0
    .kernarg_segment_align: 8
    .kernarg_segment_size: 432
    .language:       OpenCL C
    .language_version:
      - 2
      - 0
    .max_flat_workgroup_size: 512
    .name:           _Z6mk_fwd6Params
    .private_segment_fixed_size: 0
    .sgpr_count:     108
    .sgpr_spill_count: 9
    .symbol:         _Z6mk_fwd6Params.kd
    .uniform_work_group_size: 1
    .uses_dynamic_stack: false
    .vgpr_count:     251
    .vgpr_spill_count: 0
    .wavefront_size: 64
